# v020 + video stores interleaved with softmax2; all resid/out address math moved to constant SGPR base pairs + one 32-bit VGPR offset
# speedup vs baseline: 1.0243x; 1.0050x over previous
.LBB3_140:
	s_load_dwordx2 s[4:5], s[0:1], 0x30
	s_load_dwordx2 s[10:11], s[0:1], 0x0
	s_load_dwordx2 s[12:13], s[0:1], 0x28
	s_load_dwordx2 s[14:15], s[0:1], 0x38
	s_lshr_b32 s0, s2, 6
	s_add_i32 s0, s17, s0
	v_lshl_or_b32 v206, s0, 3, v1
	s_mul_i32 s0, s16, 0x180000
	v_mov_b32_e32 v207, 0
	s_add_u32 s0, s6, s0
	v_lshlrev_b32_e64 v58, 6, s23
	v_mov_b32_e32 v203, v207
	s_addc_u32 s1, s7, 0
	v_or_b32_e32 v54, v58, v160
	v_lshlrev_b32_e64 v59, 6, s3
	v_lshlrev_b64 v[50:51], 15, v[206:207]
	v_lshl_add_u64 v[52:53], s[0:1], 0, v[202:203]
	v_lshlrev_b32_e32 v206, 10, v54
	v_or_b32_e32 v56, v59, v160
	v_lshl_add_u64 v[54:55], v[52:53], 0, v[206:207]
	v_lshlrev_b32_e32 v206, 10, v56
	v_or_b32_e32 v60, 0x400, v58
	s_waitcnt lgkmcnt(0)
	s_barrier
	v_lshl_add_u64 v[56:57], v[52:53], 0, v[206:207]
	global_load_dwordx4 v[190:193], v[54:55], off
	global_load_dwordx4 v[194:197], v[56:57], off
	v_or_b32_e32 v54, v60, v160
	v_or_b32_e32 v61, 4, v160
	v_lshlrev_b32_e32 v206, 10, v54
	v_or_b32_e32 v56, v61, v58
	v_lshl_add_u64 v[54:55], v[52:53], 0, v[206:207]
	v_lshlrev_b32_e32 v206, 10, v56
	v_lshl_add_u64 v[56:57], v[52:53], 0, v[206:207]
	global_load_dwordx4 v[198:201], v[54:55], off
	global_load_dwordx4 v[174:177], v[56:57], off
	v_or_b32_e32 v54, v59, v61
	v_lshlrev_b32_e32 v206, 10, v54
	v_or_b32_e32 v56, v60, v61
	v_lshl_add_u64 v[50:51], s[10:11], 0, v[50:51]
	v_lshl_add_u64 v[54:55], v[52:53], 0, v[206:207]
	v_lshlrev_b32_e32 v206, 10, v56
	v_lshl_add_u64 v[50:51], v[50:51], 0, v[202:203]
	v_lshl_add_u64 v[52:53], v[52:53], 0, v[206:207]
	s_movk_i32 s2, 0x1000
	global_load_dwordx4 v[182:185], v[54:55], off
	global_load_dwordx4 v[186:189], v[52:53], off
	global_load_dwordx4 v[170:173], v[50:51], off
	global_load_dwordx4 v[162:165], v[50:51], off offset:1024
	global_load_dwordx4 v[154:157], v[50:51], off offset:2048
	global_load_dwordx4 v[146:149], v[50:51], off offset:3072
	v_add_co_u32_e32 v52, vcc, s2, v50
	s_movk_i32 s26, 0x2000
	s_nop 0
	v_addc_co_u32_e32 v53, vcc, 0, v51, vcc
	v_add_co_u32_e32 v50, vcc, s26, v50
	v_lshlrev_b32_e32 v1, 1, v1
	s_nop 0
	v_addc_co_u32_e32 v51, vcc, 0, v51, vcc
	global_load_dwordx4 v[166:169], v[52:53], off offset:1024
	global_load_dwordx4 v[158:161], v[52:53], off offset:2048
	global_load_dwordx4 v[178:181], v[50:51], off offset:-4096
	global_load_dwordx4 v[150:153], v[52:53], off offset:3072
	global_load_dwordx4 v[142:145], v[50:51], off
	global_load_dwordx4 v[138:141], v[50:51], off offset:1024
	global_load_dwordx4 v[134:137], v[50:51], off offset:2048
	global_load_dwordx4 v[130:133], v[50:51], off offset:3072
	v_mul_u32_u24_e32 v50, 0x6000, v205
	v_mul_u32_u24_e32 v52, 12, v208
	v_or_b32_e32 v50, v50, v202
	v_lshlrev_b32_e32 v51, 2, v204
	v_and_b32_e32 v52, 8, v52
	v_and_b32_e32 v1, 2, v1
	v_add_u32_e32 v50, 0x12000, v50
	v_or3_b32 v1, v1, v52, v51
	v_cvt_pk_bf16_f32 v18, v18, v19
	v_cvt_pk_bf16_f32 v19, v20, v21
	v_cvt_pk_bf16_f32 v20, v22, v23
	v_cvt_pk_bf16_f32 v21, v24, v25
	v_lshl_add_u32 v1, v1, 10, v50
	ds_write_b128 v1, v[18:21]
	v_cvt_pk_bf16_f32 v18, v26, v27
	v_cvt_pk_bf16_f32 v19, v28, v29
	v_cvt_pk_bf16_f32 v20, v30, v31
	v_cvt_pk_bf16_f32 v21, v32, v33
	ds_write_b128 v1, v[18:21] offset:1024
	v_mad_u32_u24 v1, v208, 3, 1
	v_lshlrev_b32_e32 v18, 2, v1
	v_lshlrev_b32_e32 v1, 1, v1
	v_and_b32_e32 v18, 24, v18
	v_and_b32_e32 v1, 2, v1
	v_or3_b32 v1, v1, v18, v51
	v_cvt_pk_bf16_f32 v2, v2, v3
	v_cvt_pk_bf16_f32 v3, v4, v5
	v_cvt_pk_bf16_f32 v4, v6, v7
	v_cvt_pk_bf16_f32 v5, v8, v9
	v_lshl_add_u32 v1, v1, 10, v50
	ds_write_b128 v1, v[2:5]
	v_cvt_pk_bf16_f32 v2, v10, v11
	v_cvt_pk_bf16_f32 v3, v12, v13
	v_cvt_pk_bf16_f32 v4, v14, v15
	v_cvt_pk_bf16_f32 v5, v16, v17
	ds_write_b128 v1, v[2:5] offset:1024
	v_mad_u32_u24 v1, v208, 3, 2
	v_lshlrev_b32_e32 v2, 2, v1
	v_lshlrev_b32_e32 v1, 1, v1
	s_lshl_b32 s2, s17, 3
	v_and_b32_e32 v2, 24, v2
	v_and_b32_e32 v1, 2, v1
	s_add_i32 s2, s22, s2
	v_or3_b32 v1, v1, v2, v51
	s_add_i32 s2, s2, 32
	v_cvt_pk_bf16_f32 v2, v34, v35
	v_cvt_pk_bf16_f32 v3, v36, v37
	v_cvt_pk_bf16_f32 v4, v38, v39
	v_cvt_pk_bf16_f32 v5, v40, v41
	v_lshl_add_u32 v1, v1, 10, v50
	s_mov_b32 s3, 0
	s_lshl_b32 s6, s23, 6
	s_and_b32 s28, s2, 0x7ffffff8
	s_lshl_b32 s2, s16, 9
	s_movk_i32 s27, 0x6000
	ds_write_b128 v1, v[2:5]
	v_cvt_pk_bf16_f32 v2, v42, v43
	v_cvt_pk_bf16_f32 v3, v44, v45
	v_cvt_pk_bf16_f32 v4, v46, v47
	v_cvt_pk_bf16_f32 v5, v48, v49
	s_mov_b32 s7, s3
	s_or_b32 s16, s2, s6
	s_mov_b32 s17, s3
	s_mov_b64 s[20:21], -1
	s_movk_i32 s29, 0x3000
	s_movk_i32 s30, 0x4000
	s_movk_i32 s31, 0x5000
	s_movk_i32 s33, 0x7000
	s_mov_b32 s34, 0x8000
	s_mov_b32 s35, 0xa000
	s_mov_b32 s36, 0xc000
	s_mov_b32 s37, 0xe000
	s_mov_b32 s38, 0xf149f2ca
	s_mov_b32 s39, 0x9000
	s_mov_b32 s40, 0xb000
	s_mov_b32 s41, 0
	ds_write_b128 v1, v[2:5] offset:1024
	s_add_u32 s44, s8, 0x2000
	s_addc_u32 s45, s9, 0
	s_add_u32 s46, s8, 0x4000
	s_addc_u32 s47, s9, 0
	s_add_u32 s48, s8, 0x6000
	s_addc_u32 s49, s9, 0
	s_add_u32 s50, s8, 0x8000
	s_addc_u32 s51, s9, 0
	s_add_u32 s52, s8, 0xa000
	s_addc_u32 s53, s9, 0
	s_add_u32 s54, s8, 0xc000
	s_addc_u32 s55, s9, 0
	s_add_u32 s56, s8, 0xe000
	s_addc_u32 s57, s9, 0
	s_add_u32 s58, s4, 0x2000
	s_addc_u32 s59, s5, 0
	s_add_u32 s60, s4, 0x4000
	s_addc_u32 s61, s5, 0
	s_add_u32 s62, s4, 0x6000
	s_addc_u32 s63, s5, 0
	s_add_u32 s64, s4, 0x8000
	s_addc_u32 s65, s5, 0
	s_add_u32 s66, s4, 0xa000
	s_addc_u32 s67, s5, 0
	s_add_u32 s68, s4, 0xc000
	s_addc_u32 s69, s5, 0
	s_add_u32 s70, s4, 0xe000
	s_addc_u32 s71, s5, 0
	s_add_u32 s72, s12, 0x2000
	s_addc_u32 s73, s13, 0
	s_add_u32 s74, s12, 0x3000
	s_addc_u32 s75, s13, 0
	s_add_u32 s76, s12, 0x9000
	s_addc_u32 s77, s13, 0
	s_add_u32 s78, s12, 0xb000
	s_addc_u32 s79, s13, 0
	s_add_u32 s80, s14, 0x2000
	s_addc_u32 s81, s15, 0
	s_add_u32 s82, s14, 0x3000
	s_addc_u32 s83, s15, 0
	s_add_u32 s84, s14, 0x9000
	s_addc_u32 s85, s15, 0
	s_add_u32 s86, s14, 0xb000
	s_addc_u32 s87, s15, 0
	s_branch .LBB3_142
.LBB3_141:
	s_mul_i32 s2, s41, 0x6000
	v_or_b32_e32 v98, s2, v206
	v_add_u32_e32 v250, 0x12000, v98
	ds_read_b128 v[98:101], v250 offset:8192
	v_cvt_pk_bf16_f32 v50, v50, v51
	v_cvt_pk_bf16_f32 v51, v52, v53
	v_cvt_pk_bf16_f32 v52, v54, v55
	v_cvt_pk_bf16_f32 v53, v56, v57
	ds_read_b128 v[54:57], v250 offset:9216
	v_cvt_pk_bf16_f32 v214, v82, v83
	v_cvt_pk_bf16_f32 v215, v84, v85
	ds_read_b128 v[82:85], v250 offset:13312
	s_waitcnt lgkmcnt(2)
	v_mfma_f32_32x32x16_bf16 v[114:129], v[98:101], v[50:53], 0
	ds_read_b128 v[98:101], v250 offset:12288
	v_cvt_pk_bf16_f32 v18, v18, v19
	v_cvt_pk_bf16_f32 v19, v20, v21
	v_cvt_pk_bf16_f32 v20, v22, v23
	v_cvt_pk_bf16_f32 v21, v24, v25
	v_cvt_pk_bf16_f32 v216, v86, v87
	v_cvt_pk_bf16_f32 v217, v88, v89
	v_cvt_pk_bf16_f32 v86, v10, v11
	s_waitcnt lgkmcnt(0)
	v_mfma_f32_32x32x16_bf16 v[98:113], v[98:101], v[50:53], 0
	v_cvt_pk_bf16_f32 v50, v58, v59
	v_cvt_pk_bf16_f32 v51, v60, v61
	v_cvt_pk_bf16_f32 v52, v62, v63
	v_cvt_pk_bf16_f32 v53, v64, v65
	ds_read_b128 v[58:61], v250 offset:10240
	v_cvt_pk_bf16_f32 v87, v12, v13
	v_cvt_pk_bf16_f32 v88, v14, v15
	v_mfma_f32_32x32x16_bf16 v[114:129], v[54:57], v[50:53], v[114:129]
	v_cvt_pk_bf16_f32 v2, v2, v3
	v_cvt_pk_bf16_f32 v3, v4, v5
	v_cvt_pk_bf16_f32 v4, v6, v7
	v_cvt_pk_bf16_f32 v5, v8, v9
	v_cvt_pk_bf16_f32 v6, v42, v43
	v_cvt_pk_bf16_f32 v7, v44, v45
	v_cvt_pk_bf16_f32 v8, v46, v47
	v_mfma_f32_32x32x16_bf16 v[98:113], v[82:85], v[50:53], v[98:113]
	ds_read_b128 v[22:25], v250 offset:14336
	ds_read_b128 v[50:53], v250 offset:11264
	ds_read_b128 v[10:13], v250
	v_cvt_pk_bf16_f32 v9, v48, v49
	v_cvt_pk_bf16_f32 v54, v90, v91
	v_cvt_pk_bf16_f32 v55, v92, v93
	v_cvt_pk_bf16_f32 v56, v94, v95
	v_cvt_pk_bf16_f32 v57, v96, v97
	s_waitcnt lgkmcnt(3)
	v_mfma_f32_32x32x16_bf16 v[114:129], v[58:61], v[18:21], v[114:129]
	v_cvt_pk_bf16_f32 v58, v34, v35
	v_cvt_pk_bf16_f32 v59, v36, v37
	ds_read_b128 v[34:37], v250 offset:15360
	v_cvt_pk_bf16_f32 v60, v38, v39
	v_cvt_pk_bf16_f32 v61, v40, v41
	v_cvt_pk_bf16_f32 v202, v66, v67
	v_cvt_pk_bf16_f32 v203, v68, v69
	s_waitcnt lgkmcnt(3)
	v_mfma_f32_32x32x16_bf16 v[98:113], v[22:25], v[18:21], v[98:113]
	v_cvt_pk_bf16_f32 v18, v26, v27
	v_cvt_pk_bf16_f32 v19, v28, v29
	v_cvt_pk_bf16_f32 v20, v30, v31
	v_cvt_pk_bf16_f32 v21, v32, v33
	v_cvt_pk_bf16_f32 v204, v70, v71
	v_cvt_pk_bf16_f32 v205, v72, v73
	v_cvt_pk_bf16_f32 v82, v74, v75
	s_waitcnt lgkmcnt(2)
	v_mfma_f32_32x32x16_bf16 v[114:129], v[50:53], v[18:21], v[114:129]
	v_cvt_pk_bf16_f32 v83, v76, v77
	v_cvt_pk_bf16_f32 v84, v78, v79
	v_cvt_pk_bf16_f32 v85, v80, v81
	s_lshl_b32 s2, s20, 6
	s_mov_b32 s41, 1
	s_mov_b64 s[20:21], 0
	s_nop 5
	v_max3_f32 v14, v114, s38, v115
	s_waitcnt lgkmcnt(0)
	v_mfma_f32_32x32x16_bf16 v[98:113], v[34:37], v[18:21], v[98:113]
	ds_read_b128 v[50:53], v250 offset:1024
	ds_read_b128 v[18:21], v250 offset:4096
	ds_read_b128 v[62:65], v250 offset:5120
	v_max3_f32 v14, v14, v116, v117
	v_max3_f32 v14, v14, v118, v119
	v_max3_f32 v14, v14, v120, v121
	v_max3_f32 v14, v14, v122, v123
	v_max3_f32 v14, v14, v124, v125
	v_max3_f32 v14, v14, v126, v127
	v_mfma_f32_32x32x16_bf16 v[34:49], v[214:217], v[10:13], 0
	v_max3_f32 v14, v14, v128, v129
	s_nop 0
	v_max3_f32 v14, v14, v98, v99
	v_max3_f32 v14, v14, v100, v101
	v_max3_f32 v14, v14, v102, v103
	v_max3_f32 v14, v14, v104, v105
	v_max3_f32 v14, v14, v106, v107
	v_max3_f32 v14, v14, v108, v109
	s_waitcnt lgkmcnt(1)
	v_mfma_f32_32x32x16_bf16 v[18:33], v[214:217], v[18:21], 0
	v_max3_f32 v14, v14, v110, v111
	v_max3_f32 v14, v14, v112, v113
	v_mov_b32_e32 v15, v14
	ds_read_b128 v[10:13], v250 offset:2048
	ds_read_b128 v[66:69], v250 offset:3072
	ds_read_b128 v[70:73], v250 offset:6144
	ds_read_b128 v[74:77], v250 offset:7168
	v_permlane32_swap_b32_e32 v14, v15
	v_max_f32_e32 v15, v15, v15
	v_mfma_f32_32x32x16_bf16 v[34:49], v[54:57], v[50:53], v[34:49]
	v_max_f32_e32 v14, v14, v14
	v_max_f32_e32 v14, v14, v15
	v_mul_f32_e32 v14, 0xbe38aa3b, v14
	v_fmamk_f32 v15, v114, 0x3e38aa3b, v14
	v_fmamk_f32 v50, v118, 0x3e38aa3b, v14
	v_exp_f32_e32 v50, v50
	v_fmamk_f32 v51, v119, 0x3e38aa3b, v14
	s_waitcnt lgkmcnt(4)
	v_mfma_f32_32x32x16_bf16 v[18:33], v[54:57], v[62:65], v[18:33]
	v_exp_f32_e32 v51, v51
	v_fmamk_f32 v52, v120, 0x3e38aa3b, v14
	v_exp_f32_e32 v52, v52
	v_fmamk_f32 v53, v121, 0x3e38aa3b, v14
	v_exp_f32_e32 v53, v53
	v_fmamk_f32 v109, v109, 0x3e38aa3b, v14
	s_waitcnt lgkmcnt(3)
	v_mfma_f32_32x32x16_bf16 v[34:49], v[58:61], v[10:13], v[34:49]
	v_exp_f32_e32 v10, v15
	v_fmamk_f32 v11, v115, 0x3e38aa3b, v14
	v_exp_f32_e32 v11, v11
	v_fmamk_f32 v12, v116, 0x3e38aa3b, v14
	v_exp_f32_e32 v12, v12
	v_fmamk_f32 v15, v117, 0x3e38aa3b, v14
	v_exp_f32_e32 v15, v15
	s_waitcnt lgkmcnt(1)
	v_mfma_f32_32x32x16_bf16 v[18:33], v[58:61], v[70:73], v[18:33]
	v_add_f32_e32 v13, 0, v10
	v_add_f32_e32 v13, v13, v11
	v_add_f32_e32 v13, v13, v12
	v_add_f32_e32 v13, v13, v15
	v_add_f32_e32 v13, v13, v50
	v_add_f32_e32 v13, v13, v51
	v_cvt_pk_bf16_f32 v10, v10, v11
	v_mfma_f32_32x32x16_bf16 v[34:49], v[6:9], v[66:69], v[34:49]
	v_cvt_pk_bf16_f32 v11, v12, v15
	v_cvt_pk_bf16_f32 v12, v50, v51
	s_waitcnt lgkmcnt(0)
	v_mfma_f32_32x32x16_bf16 v[18:33], v[6:9], v[74:77], v[18:33]
	v_fmamk_f32 v6, v122, 0x3e38aa3b, v14
	v_exp_f32_e32 v89, v6
	v_fmamk_f32 v6, v123, 0x3e38aa3b, v14
	v_exp_f32_e32 v94, v6
	v_fmamk_f32 v7, v124, 0x3e38aa3b, v14
	v_add_f32_e32 v6, v13, v52
	v_exp_f32_e32 v95, v7
	v_fmamk_f32 v7, v125, 0x3e38aa3b, v14
	v_add_f32_e32 v6, v6, v53
	v_exp_f32_e32 v96, v7
	v_fmamk_f32 v7, v126, 0x3e38aa3b, v14
	v_add_f32_e32 v6, v6, v89
	v_exp_f32_e32 v97, v7
	v_fmamk_f32 v7, v127, 0x3e38aa3b, v14
	v_add_f32_e32 v6, v6, v94
	v_exp_f32_e32 v114, v7
	v_fmamk_f32 v7, v128, 0x3e38aa3b, v14
	v_add_f32_e32 v6, v6, v95
	v_exp_f32_e32 v115, v7
	v_fmamk_f32 v7, v129, 0x3e38aa3b, v14
	v_add_f32_e32 v6, v6, v96
	v_exp_f32_e32 v116, v7
	v_fmamk_f32 v7, v98, 0x3e38aa3b, v14
	v_add_f32_e32 v6, v6, v97
	v_exp_f32_e32 v98, v7
	v_fmamk_f32 v7, v99, 0x3e38aa3b, v14
	v_add_f32_e32 v6, v6, v114
	v_exp_f32_e32 v99, v7
	v_fmamk_f32 v7, v100, 0x3e38aa3b, v14
	v_add_f32_e32 v6, v6, v115
	v_exp_f32_e32 v100, v7
	v_fmamk_f32 v7, v101, 0x3e38aa3b, v14
	v_add_f32_e32 v6, v6, v116
	v_exp_f32_e32 v101, v7
	v_fmamk_f32 v7, v102, 0x3e38aa3b, v14
	v_add_f32_e32 v6, v6, v98
	v_exp_f32_e32 v102, v7
	v_fmamk_f32 v7, v103, 0x3e38aa3b, v14
	v_add_f32_e32 v6, v6, v99
	v_exp_f32_e32 v103, v7
	v_add_f32_e32 v6, v6, v100
	v_add_f32_e32 v6, v6, v101
	v_add_f32_e32 v6, v6, v102
	v_add_f32_e32 v54, v6, v103
	v_fmamk_f32 v6, v104, 0x3e38aa3b, v14
	v_exp_f32_e32 v104, v6
	ds_read_b128 v[6:9], v250 offset:16384
	v_fmamk_f32 v13, v105, 0x3e38aa3b, v14
	v_exp_f32_e32 v105, v13
	v_cvt_pk_bf16_f32 v13, v52, v53
	ds_read_b128 v[50:53], v250 offset:18432
	ds_read_b128 v[90:93], v250 offset:17408
	s_waitcnt lgkmcnt(2)
	v_mfma_f32_32x32x16_bf16 v[66:81], v[6:9], v[10:13], 0
	v_add_f32_e32 v6, v54, v104
	v_add_f32_e32 v15, v6, v105
	v_fmamk_f32 v6, v106, 0x3e38aa3b, v14
	v_exp_f32_e32 v106, v6
	v_fmamk_f32 v6, v107, 0x3e38aa3b, v14
	v_exp_f32_e32 v107, v6
	ds_read_b128 v[6:9], v250 offset:19456
	s_waitcnt lgkmcnt(2)
	v_mfma_f32_32x32x16_bf16 v[50:65], v[50:53], v[10:13], 0
	v_fmamk_f32 v10, v108, 0x3e38aa3b, v14
	v_exp_f32_e32 v108, v10
	v_cvt_pk_bf16_f32 v10, v89, v94
	v_cvt_pk_bf16_f32 v11, v95, v96
	v_cvt_pk_bf16_f32 v12, v97, v114
	v_cvt_pk_bf16_f32 v13, v115, v116
	v_fmamk_f32 v94, v110, 0x3e38aa3b, v14
	v_exp_f32_e32 v89, v109
	s_waitcnt lgkmcnt(1)
	v_mfma_f32_32x32x16_bf16 v[66:81], v[90:93], v[10:13], v[66:81]
	ds_read_b128 v[90:93], v250 offset:20480
	v_exp_f32_e32 v109, v94
	v_add_f32_e32 v15, v15, v106
	v_add_f32_e32 v15, v15, v107
	v_add_f32_e32 v15, v15, v108
	v_add_f32_e32 v15, v15, v89
	v_add_f32_e32 v15, v15, v109
	s_waitcnt lgkmcnt(1)
	v_mfma_f32_32x32x16_bf16 v[50:65], v[6:9], v[10:13], v[50:65]
	v_cvt_pk_bf16_f32 v6, v98, v99
	v_cvt_pk_bf16_f32 v7, v100, v101
	v_cvt_pk_bf16_f32 v8, v102, v103
	v_cvt_pk_bf16_f32 v9, v104, v105
	ds_read_b128 v[10:13], v250 offset:22528
	ds_read_b128 v[94:97], v250 offset:21504
	s_waitcnt lgkmcnt(2)
	v_mfma_f32_32x32x16_bf16 v[66:81], v[90:93], v[6:9], v[66:81]
	v_fmamk_f32 v90, v111, 0x3e38aa3b, v14
	v_exp_f32_e32 v98, v90
	v_fmamk_f32 v90, v112, 0x3e38aa3b, v14
	v_fmac_f32_e32 v14, 0x3e38aa3b, v113
	v_exp_f32_e32 v99, v90
	ds_read_b128 v[90:93], v250 offset:23552
	v_add_f32_e32 v15, v15, v98
	s_waitcnt lgkmcnt(2)
	v_mfma_f32_32x32x16_bf16 v[50:65], v[10:13], v[6:9], v[50:65]
	v_exp_f32_e32 v11, v14
	v_add_f32_e32 v10, v15, v99
	v_cvt_pk_bf16_f32 v6, v106, v107
	v_cvt_pk_bf16_f32 v7, v108, v89
	v_cvt_pk_bf16_f32 v8, v109, v98
	v_cvt_pk_bf16_f32 v9, v99, v11
	v_add_f32_e32 v10, v10, v11
	v_mov_b32_e32 v11, v10
	s_waitcnt lgkmcnt(1)
	v_mfma_f32_32x32x16_bf16 v[66:81], v[94:97], v[6:9], v[66:81]
	v_permlane32_swap_b32_e32 v10, v11
	v_add_f32_e32 v10, v10, v11
	v_rcp_f32_e32 v101, v10
	v_cvt_pk_bf16_f32 v89, v16, v17
	v_ashrrev_i32_e32 v118, 3, v210
	v_and_b32_e32 v118, 0xffffffe0, v118
	v_bfe_u32 v119, v210, 6, 1
	v_add_u32_e32 v118, s16, v118
	v_lshl_or_b32 v118, v119, 4, v118
	v_or_b32_e32 v118, v118, v211
	v_lshlrev_b32_e32 v118, 10, v118
	v_add_u32_e32 v118, s2, v118
	v_bfe_u32 v119, v210, 7, 1
	v_lshl_or_b32 v118, v119, 5, v118
	v_or_b32_e32 v118, v118, v1
	v_lshlrev_b32_e32 v118, 2, v118
	global_load_dword v110, v118, s[12:13]
	global_load_dword v111, v118, s[72:73] offset:-4096
	global_load_dword v112, v118, s[72:73]
	global_load_dword v113, v118, s[76:77] offset:-4096
	global_load_dword v114, v118, s[76:77]
	global_load_dword v115, v118, s[78:79] offset:-4096
	global_load_dword v116, v118, s[78:79]
	global_load_dword v117, v118, s[74:75]
	s_nop 6
	s_waitcnt vmcnt(35)
	v_fmac_f32_e32 v245, v101, v70
	s_waitcnt lgkmcnt(0)
	v_mfma_f32_32x32x16_bf16 v[50:65], v[90:93], v[6:9], v[50:65]
	s_waitcnt vmcnt(34)
	v_fmac_f32_e32 v243, v101, v71
	s_waitcnt vmcnt(33)
	v_fmac_f32_e32 v241, v101, v72
	s_waitcnt vmcnt(32)
	v_fmac_f32_e32 v239, v101, v73
	global_store_dword v252, v245, s[58:59] nt
	global_store_dword v252, v243, s[58:59] offset:1024 nt
	global_store_dword v252, v241, s[58:59] offset:2048 nt
	global_store_dword v252, v239, s[58:59] offset:3072 nt
	v_max3_f32 v6, v34, s38, v35
	v_max3_f32 v6, v6, v36, v37
	v_max3_f32 v6, v6, v38, v39
	v_max3_f32 v6, v6, v40, v41
	v_max3_f32 v7, v18, s38, v19
	v_max3_f32 v6, v6, v42, v43
	v_max3_f32 v7, v7, v20, v21
	v_max3_f32 v6, v6, v44, v45
	v_max3_f32 v7, v7, v22, v23
	v_max3_f32 v6, v6, v46, v47
	v_max3_f32 v7, v7, v24, v25
	v_max3_f32 v6, v6, v48, v49
	v_max3_f32 v7, v7, v26, v27
	v_max3_f32 v7, v7, v28, v29
	v_mov_b32_e32 v8, v6
	s_waitcnt vmcnt(35)
	v_fmac_f32_e32 v244, v101, v74
	s_waitcnt vmcnt(34)
	v_fmac_f32_e32 v242, v101, v75
	s_waitcnt vmcnt(33)
	v_fmac_f32_e32 v240, v101, v76
	s_waitcnt vmcnt(32)
	v_fmac_f32_e32 v238, v101, v77
	global_store_dword v252, v244, s[60:61] nt
	global_store_dword v252, v242, s[60:61] offset:1024 nt
	global_store_dword v252, v240, s[60:61] offset:2048 nt
	global_store_dword v252, v238, s[60:61] offset:3072 nt
	v_max3_f32 v7, v7, v30, v31
	s_nop 0
	v_permlane32_swap_b32_e32 v6, v8
	v_max3_f32 v7, v7, v32, v33
	v_max_f32_e32 v8, v8, v8
	v_max_f32_e32 v6, v6, v6
	v_max_f32_e32 v90, v6, v8
	v_mov_b32_e32 v6, v7
	s_nop 1
	v_permlane32_swap_b32_e32 v7, v6
	v_mul_f32_e32 v8, 0xbe38aa3b, v90
	v_fmamk_f32 v9, v34, 0x3e38aa3b, v8
	v_max_f32_e32 v6, v6, v6
	v_max_f32_e32 v7, v7, v7
	v_exp_f32_e32 v9, v9
	s_waitcnt vmcnt(35)
	v_fmac_f32_e32 v236, v101, v78
	s_waitcnt vmcnt(34)
	v_fmac_f32_e32 v234, v101, v79
	s_waitcnt vmcnt(31)
	v_fmac_f32_e32 v232, v101, v80
	s_waitcnt vmcnt(30)
	v_fmac_f32_e32 v230, v101, v81
	global_store_dword v252, v236, s[62:63] nt
	global_store_dword v252, v234, s[62:63] offset:1024 nt
	global_store_dword v252, v232, s[62:63] offset:2048 nt
	global_store_dword v252, v230, s[62:63] offset:3072 nt
	v_max_f32_e32 v91, v7, v6
	v_fmamk_f32 v7, v35, 0x3e38aa3b, v8
	v_exp_f32_e32 v7, v7
	v_fmamk_f32 v10, v36, 0x3e38aa3b, v8
	v_exp_f32_e32 v10, v10
	v_fmamk_f32 v11, v37, 0x3e38aa3b, v8
	v_exp_f32_e32 v11, v11
	v_fmamk_f32 v12, v38, 0x3e38aa3b, v8
	v_add_f32_e32 v6, 0, v9
	v_exp_f32_e32 v12, v12
	v_fmamk_f32 v13, v39, 0x3e38aa3b, v8
	v_add_f32_e32 v6, v6, v7
	v_exp_f32_e32 v13, v13
	v_fmamk_f32 v14, v40, 0x3e38aa3b, v8
	v_add_f32_e32 v6, v6, v10
	v_fmac_f32_e32 v237, v101, v50
	v_fmac_f32_e32 v235, v101, v51
	s_waitcnt vmcnt(33)
	v_fmac_f32_e32 v233, v101, v52
	s_waitcnt vmcnt(32)
	v_fmac_f32_e32 v231, v101, v53
	global_store_dword v252, v237, s[64:65] nt
	global_store_dword v252, v235, s[64:65] offset:1024 nt
	global_store_dword v252, v233, s[64:65] offset:2048 nt
	global_store_dword v252, v231, s[64:65] offset:3072 nt
	v_exp_f32_e32 v14, v14
	v_fmamk_f32 v15, v41, 0x3e38aa3b, v8
	v_fmamk_f32 v16, v42, 0x3e38aa3b, v8
	v_add_f32_e32 v6, v6, v11
	v_exp_f32_e32 v15, v15
	v_exp_f32_e32 v92, v16
	v_fmamk_f32 v16, v43, 0x3e38aa3b, v8
	v_add_f32_e32 v6, v6, v12
	v_exp_f32_e32 v93, v16
	v_fmamk_f32 v16, v44, 0x3e38aa3b, v8
	v_add_f32_e32 v6, v6, v13
	v_exp_f32_e32 v94, v16
	v_fmamk_f32 v16, v45, 0x3e38aa3b, v8
	v_add_f32_e32 v6, v6, v14
	v_exp_f32_e32 v95, v16
	s_waitcnt vmcnt(35)
	v_fmac_f32_e32 v228, v101, v54
	s_waitcnt vmcnt(34)
	v_fmac_f32_e32 v226, v101, v55
	s_waitcnt vmcnt(33)
	v_fmac_f32_e32 v224, v101, v56
	s_waitcnt vmcnt(32)
	v_fmac_f32_e32 v222, v101, v57
	global_store_dword v252, v228, s[66:67] nt
	global_store_dword v252, v226, s[66:67] offset:1024 nt
	global_store_dword v252, v224, s[66:67] offset:2048 nt
	global_store_dword v252, v222, s[66:67] offset:3072 nt
	v_fmamk_f32 v16, v46, 0x3e38aa3b, v8
	v_add_f32_e32 v6, v6, v15
	v_exp_f32_e32 v96, v16
	v_fmamk_f32 v16, v47, 0x3e38aa3b, v8
	v_add_f32_e32 v6, v6, v92
	v_exp_f32_e32 v97, v16
	v_fmamk_f32 v16, v48, 0x3e38aa3b, v8
	v_add_f32_e32 v6, v6, v93
	v_exp_f32_e32 v98, v16
	v_fmac_f32_e32 v8, 0x3e38aa3b, v49
	v_mul_f32_e32 v16, 0xbe38aa3b, v91
	v_add_f32_e32 v6, v6, v94
	v_exp_f32_e32 v99, v8
	v_fmamk_f32 v8, v18, 0x3e38aa3b, v16
	v_add_f32_e32 v6, v6, v95
	v_fmac_f32_e32 v249, v101, v66
	v_fmac_f32_e32 v248, v101, v67
	v_fmac_f32_e32 v247, v101, v68
	v_fmac_f32_e32 v246, v101, v69
	global_store_dword v252, v249, s[4:5] nt
	global_store_dword v252, v248, s[4:5] offset:1024 nt
	global_store_dword v252, v247, s[4:5] offset:2048 nt
	global_store_dword v252, v246, s[4:5] offset:3072 nt
	v_exp_f32_e32 v17, v8
	v_fmamk_f32 v8, v19, 0x3e38aa3b, v16
	v_add_f32_e32 v6, v6, v96
	v_exp_f32_e32 v18, v8
	v_fmamk_f32 v8, v20, 0x3e38aa3b, v16
	v_add_f32_e32 v6, v6, v97
	v_exp_f32_e32 v19, v8
	v_fmamk_f32 v8, v21, 0x3e38aa3b, v16
	v_add_f32_e32 v6, v6, v98
	v_exp_f32_e32 v20, v8
	v_fmamk_f32 v8, v22, 0x3e38aa3b, v16
	v_add_f32_e32 v100, v6, v99
	v_add_f32_e32 v6, 0, v17
	v_exp_f32_e32 v21, v8
	s_waitcnt vmcnt(35)
	v_fmac_f32_e32 v221, v101, v62
	s_waitcnt vmcnt(34)
	v_fmac_f32_e32 v220, v101, v63
	s_waitcnt vmcnt(33)
	v_fmac_f32_e32 v219, v101, v64
	s_waitcnt vmcnt(32)
	v_fmac_f32_e32 v218, v101, v65
	global_store_dword v252, v221, s[70:71] nt
	global_store_dword v252, v220, s[70:71] offset:1024 nt
	global_store_dword v252, v219, s[70:71] offset:2048 nt
	global_store_dword v252, v218, s[70:71] offset:3072 nt
	v_fmamk_f32 v8, v23, 0x3e38aa3b, v16
	v_add_f32_e32 v6, v6, v18
	v_exp_f32_e32 v22, v8
	v_fmamk_f32 v8, v24, 0x3e38aa3b, v16
	v_add_f32_e32 v6, v6, v19
	v_exp_f32_e32 v23, v8
	v_fmamk_f32 v8, v25, 0x3e38aa3b, v16
	v_add_f32_e32 v6, v6, v20
	v_exp_f32_e32 v24, v8
	v_fmamk_f32 v8, v26, 0x3e38aa3b, v16
	v_add_f32_e32 v6, v6, v21
	v_exp_f32_e32 v25, v8
	v_add_f32_e32 v6, v6, v22
	v_add_f32_e32 v6, v6, v23
	v_fmac_f32_e32 v229, v101, v58
	v_fmac_f32_e32 v227, v101, v59
	v_fmac_f32_e32 v225, v101, v60
	v_fmac_f32_e32 v223, v101, v61
	global_store_dword v252, v229, s[68:69] nt
	global_store_dword v252, v227, s[68:69] offset:1024 nt
	global_store_dword v252, v225, s[68:69] offset:2048 nt
	global_store_dword v252, v223, s[68:69] offset:3072 nt
	v_add_f32_e32 v6, v6, v24
	v_add_f32_e32 v26, v6, v25
	v_fmamk_f32 v6, v27, 0x3e38aa3b, v16
	v_exp_f32_e32 v27, v6
	v_cvt_pk_bf16_f32 v6, v9, v7
	v_cvt_pk_bf16_f32 v7, v10, v11
	v_fmamk_f32 v10, v28, 0x3e38aa3b, v16
	v_cvt_pk_bf16_f32 v9, v14, v15
	v_exp_f32_e32 v28, v10
	v_fmamk_f32 v14, v29, 0x3e38aa3b, v16
	v_cvt_pk_bf16_f32 v8, v12, v13
	v_cvt_pk_bf16_f32 v13, v23, v24
	v_exp_f32_e32 v23, v14
	v_fmamk_f32 v14, v30, 0x3e38aa3b, v16
	v_mfma_f32_32x32x16_bf16 v[66:81], v[202:205], v[6:9], 0
	v_exp_f32_e32 v24, v14
	v_add_f32_e32 v14, v26, v27
	v_add_f32_e32 v14, v14, v28
	v_add_f32_e32 v14, v14, v23
	v_cvt_pk_bf16_f32 v10, v17, v18
	v_cvt_pk_bf16_f32 v11, v19, v20
	v_cvt_pk_bf16_f32 v12, v21, v22
	v_mfma_f32_32x32x16_bf16 v[34:49], v[2:5], v[6:9], 0
	v_fmamk_f32 v6, v31, 0x3e38aa3b, v16
	v_exp_f32_e32 v26, v6
	v_add_f32_e32 v14, v14, v24
	v_fmamk_f32 v6, v32, 0x3e38aa3b, v16
	v_fmac_f32_e32 v16, 0x3e38aa3b, v33
	v_exp_f32_e32 v29, v6
	v_exp_f32_e32 v30, v16
	v_mfma_f32_32x32x16_bf16 v[50:65], v[202:205], v[10:13], 0
	v_add_f32_e32 v18, v14, v26
	v_mov_b32_e32 v22, v100
	s_nop 1
	v_permlane32_swap_b32_e32 v100, v22
	v_add_f32_e32 v32, v100, v22
	v_cvt_pk_bf16_f32 v22, v25, v27
	v_cvt_pk_bf16_f32 v23, v28, v23
	v_mfma_f32_32x32x16_bf16 v[2:17], v[2:5], v[10:13], 0
	v_cvt_pk_bf16_f32 v24, v24, v26
	v_cvt_pk_bf16_f32 v25, v29, v30
	v_lshlrev_b32_e32 v26, 2, v213
	v_lshl_or_b32 v27, v212, 10, v26
	v_add_f32_e32 v18, v18, v29
	v_add_u32_e32 v28, 0x10000, v27
	v_add_f32_e32 v31, v18, v30
	v_mfma_f32_32x32x16_bf16 v[2:17], v[86:89], v[22:25], v[2:17]
	ds_write_b32 v28, v90
	v_add_u32_e32 v28, 0x10100, v27
	v_cvt_pk_bf16_f32 v18, v92, v93
	v_cvt_pk_bf16_f32 v19, v94, v95
	v_cvt_pk_bf16_f32 v20, v96, v97
	v_cvt_pk_bf16_f32 v21, v98, v99
	ds_write_b32 v28, v32
	v_mov_b32_e32 v28, v31
	v_mfma_f32_32x32x16_bf16 v[66:81], v[82:85], v[18:21], v[66:81]
	s_nop 0
	v_permlane32_swap_b32_e32 v31, v28
	s_nop 0
	v_cvt_pk_bf16_f32 v2, v2, v3
	v_cvt_pk_bf16_f32 v3, v4, v5
	v_cvt_pk_bf16_f32 v4, v6, v7
	v_cvt_pk_bf16_f32 v5, v8, v9
	v_mfma_f32_32x32x16_bf16 v[34:49], v[86:89], v[18:21], v[34:49]
	v_add_u32_e32 v19, 0x10200, v27
	v_add_f32_e32 v18, v31, v28
	ds_write_b32 v19, v91
	v_add_u32_e32 v19, 0x10300, v27
	ds_write_b32 v19, v18
	v_cvt_pk_bf16_f32 v18, v66, v67
	v_cvt_pk_bf16_f32 v19, v68, v69
	v_mfma_f32_32x32x16_bf16 v[50:65], v[82:85], v[22:25], v[50:65]
	v_lshl_or_b32 v22, v212, 13, v206
	ds_write_b128 v22, v[2:5] offset:6144
	v_cvt_pk_bf16_f32 v2, v10, v11
	v_cvt_pk_bf16_f32 v3, v12, v13
	v_cvt_pk_bf16_f32 v4, v14, v15
	v_cvt_pk_bf16_f32 v5, v16, v17
	ds_write_b128 v22, v[2:5] offset:7168
	v_bfe_u32 v16, v210, 6, 1
	v_ashrrev_i32_e32 v14, 7, v210
	v_and_b32_e32 v15, 1, v14
	v_cvt_pk_bf16_f32 v20, v70, v71
	v_cvt_pk_bf16_f32 v21, v72, v73
	ds_write_b128 v22, v[18:21]
	v_cvt_pk_bf16_f32 v18, v74, v75
	v_cvt_pk_bf16_f32 v19, v76, v77
	v_cvt_pk_bf16_f32 v20, v78, v79
	v_cvt_pk_bf16_f32 v21, v80, v81
	ds_write_b128 v22, v[18:21] offset:1024
	v_cvt_pk_bf16_f32 v18, v50, v51
	v_cvt_pk_bf16_f32 v19, v52, v53
	v_cvt_pk_bf16_f32 v20, v54, v55
	v_cvt_pk_bf16_f32 v21, v56, v57
	ds_write_b128 v22, v[18:21] offset:2048
	v_cvt_pk_bf16_f32 v18, v58, v59
	v_cvt_pk_bf16_f32 v19, v60, v61
	v_cvt_pk_bf16_f32 v20, v62, v63
	v_cvt_pk_bf16_f32 v21, v64, v65
	ds_write_b128 v22, v[18:21] offset:3072
	v_cvt_pk_bf16_f32 v18, v34, v35
	v_cvt_pk_bf16_f32 v19, v36, v37
	v_cvt_pk_bf16_f32 v20, v38, v39
	v_cvt_pk_bf16_f32 v21, v40, v41
	ds_write_b128 v22, v[18:21] offset:4096
	v_cvt_pk_bf16_f32 v18, v42, v43
	v_cvt_pk_bf16_f32 v19, v44, v45
	v_cvt_pk_bf16_f32 v20, v46, v47
	v_cvt_pk_bf16_f32 v21, v48, v49
	ds_write_b128 v22, v[18:21] offset:5120
	v_lshl_or_b32 v4, v15, 9, v26
	v_or_b32_e32 v5, 0x10000, v4
	v_or_b32_e32 v12, 0x10d00, v4
	s_waitcnt lgkmcnt(0)
	s_barrier
	v_or_b32_e32 v6, 0x10100, v4
	v_or_b32_e32 v7, 0x10400, v4
	v_or_b32_e32 v8, 0x10500, v4
	v_or_b32_e32 v9, 0x10800, v4
	v_or_b32_e32 v10, 0x10900, v4
	v_or_b32_e32 v11, 0x10c00, v4
	ds_read_b32 v5, v5
	ds_read_b32 v13, v6
	ds_read_b32 v15, v7
	ds_read_b32 v24, v8
	ds_read_b32 v25, v9
	ds_read_b32 v26, v10
	ds_read_b32 v27, v11
	ds_read_b32 v12, v12
	v_or_b32_e32 v6, 0x11000, v4
	v_or_b32_e32 v7, 0x11100, v4
	v_or_b32_e32 v8, 0x11400, v4
	v_or_b32_e32 v9, 0x11500, v4
	v_or_b32_e32 v10, 0x11800, v4
	v_or_b32_e32 v11, 0x11900, v4
	v_or_b32_e32 v28, 0x11c00, v4
	v_or_b32_e32 v4, 0x11d00, v4
	ds_read_b32 v29, v6
	ds_read_b32 v30, v7
	ds_read_b32 v31, v8
	ds_read_b32 v32, v9
	ds_read_b32 v33, v10
	ds_read_b32 v34, v11
	ds_read_b32 v28, v28
	ds_read_b32 v35, v4
	s_waitcnt lgkmcnt(13)
	v_max_f32_e32 v4, v15, v15
	v_max_f32_e32 v6, v5, v5
	v_max_f32_e32 v4, v6, v4
	s_waitcnt lgkmcnt(9)
	v_max3_f32 v4, v4, v25, v27
	s_waitcnt lgkmcnt(5)
	v_max3_f32 v4, v4, v29, v31
	s_waitcnt lgkmcnt(1)
	v_max3_f32 v36, v4, v33, v28
	v_sub_f32_e32 v4, v5, v36
	v_mul_f32_e32 v4, 0x3e38aa3b, v4
	v_exp_f32_e32 v37, v4
	v_lshlrev_b32_e32 v4, 11, v14
	v_lshlrev_b32_e32 v5, 10, v16
	v_or3_b32 v14, v206, v4, v5
	ds_read_b128 v[4:7], v14
	ds_read_b128 v[8:11], v14 offset:8192
	v_fma_f32 v13, v13, v37, 0
	s_waitcnt lgkmcnt(1)
	v_lshlrev_b32_e32 v16, 16, v4
	v_and_b32_e32 v4, 0xffff0000, v4
	v_fma_f32 v38, v37, v4, 0
	v_lshlrev_b32_e32 v4, 16, v5
	v_fma_f32 v39, v37, v4, 0
	v_and_b32_e32 v4, 0xffff0000, v5
	v_sub_f32_e32 v5, v15, v36
	v_fma_f32 v40, v37, v4, 0
	v_lshlrev_b32_e32 v4, 16, v6
	v_mul_f32_e32 v5, 0x3e38aa3b, v5
	v_fma_f32 v41, v37, v4, 0
	v_and_b32_e32 v4, 0xffff0000, v6
	v_exp_f32_e32 v15, v5
	v_fma_f32 v42, v37, v4, 0
	v_lshlrev_b32_e32 v4, 16, v7
	v_fma_f32 v43, v37, v4, 0
	v_and_b32_e32 v4, 0xffff0000, v7
	v_fma_f32 v16, v37, v16, 0
	v_fma_f32 v37, v37, v4, 0
	s_waitcnt lgkmcnt(0)
	v_lshlrev_b32_e32 v4, 16, v8
	v_fmac_f32_e32 v16, v15, v4
	v_and_b32_e32 v4, 0xffff0000, v8
	v_fmac_f32_e32 v38, v15, v4
	v_lshlrev_b32_e32 v4, 16, v9
	v_fmac_f32_e32 v39, v15, v4
	v_and_b32_e32 v4, 0xffff0000, v9
	v_fmac_f32_e32 v40, v15, v4
	v_lshlrev_b32_e32 v4, 16, v10
	v_fmac_f32_e32 v41, v15, v4
	v_and_b32_e32 v4, 0xffff0000, v10
	v_fmac_f32_e32 v42, v15, v4
	v_lshlrev_b32_e32 v4, 16, v11
	v_fmac_f32_e32 v43, v15, v4
	v_sub_f32_e32 v4, v25, v36
	v_mul_f32_e32 v4, 0x3e38aa3b, v4
	v_fmac_f32_e32 v13, v24, v15
	v_exp_f32_e32 v24, v4
	ds_read_b128 v[4:7], v14 offset:16384
	v_and_b32_e32 v8, 0xffff0000, v11
	v_fmac_f32_e32 v37, v15, v8
	ds_read_b128 v[8:11], v14 offset:24576
	v_fmac_f32_e32 v13, v26, v24
	s_waitcnt lgkmcnt(1)
	v_lshlrev_b32_e32 v15, 16, v4
	v_and_b32_e32 v4, 0xffff0000, v4
	v_fmac_f32_e32 v38, v24, v4
	v_lshlrev_b32_e32 v4, 16, v5
	v_fmac_f32_e32 v39, v24, v4
	v_and_b32_e32 v4, 0xffff0000, v5
	v_sub_f32_e32 v5, v27, v36
	v_fmac_f32_e32 v40, v24, v4
	v_lshlrev_b32_e32 v4, 16, v6
	v_mul_f32_e32 v5, 0x3e38aa3b, v5
	v_fmac_f32_e32 v16, v24, v15
	v_fmac_f32_e32 v41, v24, v4
	v_and_b32_e32 v4, 0xffff0000, v6
	v_exp_f32_e32 v15, v5
	v_fmac_f32_e32 v42, v24, v4
	v_lshlrev_b32_e32 v4, 16, v7
	v_fmac_f32_e32 v43, v24, v4
	v_and_b32_e32 v4, 0xffff0000, v7
	v_fmac_f32_e32 v37, v24, v4
	s_waitcnt lgkmcnt(0)
	v_lshlrev_b32_e32 v4, 16, v8
	v_fmac_f32_e32 v16, v15, v4
	v_and_b32_e32 v4, 0xffff0000, v8
	v_fmac_f32_e32 v38, v15, v4
	v_lshlrev_b32_e32 v4, 16, v9
	v_fmac_f32_e32 v39, v15, v4
	v_and_b32_e32 v4, 0xffff0000, v9
	v_fmac_f32_e32 v40, v15, v4
	v_lshlrev_b32_e32 v4, 16, v10
	v_fmac_f32_e32 v41, v15, v4
	v_and_b32_e32 v4, 0xffff0000, v10
	v_fmac_f32_e32 v42, v15, v4
	v_lshlrev_b32_e32 v4, 16, v11
	v_fmac_f32_e32 v43, v15, v4
	v_sub_f32_e32 v4, v29, v36
	v_mul_f32_e32 v4, 0x3e38aa3b, v4
	v_fmac_f32_e32 v13, v12, v15
	v_exp_f32_e32 v12, v4
	ds_read_b128 v[4:7], v14 offset:32768
	v_and_b32_e32 v8, 0xffff0000, v11
	v_fmac_f32_e32 v37, v15, v8
	ds_read_b128 v[8:11], v14 offset:40960
	v_fmac_f32_e32 v13, v30, v12
	s_waitcnt lgkmcnt(1)
	v_lshlrev_b32_e32 v15, 16, v4
	v_and_b32_e32 v4, 0xffff0000, v4
	v_fmac_f32_e32 v38, v12, v4
	v_lshlrev_b32_e32 v4, 16, v5
	v_fmac_f32_e32 v39, v12, v4
	v_and_b32_e32 v4, 0xffff0000, v5
	v_sub_f32_e32 v5, v31, v36
	v_fmac_f32_e32 v40, v12, v4
	v_lshlrev_b32_e32 v4, 16, v6
	v_mul_f32_e32 v5, 0x3e38aa3b, v5
	v_fmac_f32_e32 v16, v12, v15
	v_fmac_f32_e32 v41, v12, v4
	v_and_b32_e32 v4, 0xffff0000, v6
	v_exp_f32_e32 v15, v5
	v_fmac_f32_e32 v42, v12, v4
	v_lshlrev_b32_e32 v4, 16, v7
	v_fmac_f32_e32 v43, v12, v4
	v_and_b32_e32 v4, 0xffff0000, v7
	v_fmac_f32_e32 v37, v12, v4
	s_waitcnt lgkmcnt(0)
	v_lshlrev_b32_e32 v4, 16, v8
	v_fmac_f32_e32 v16, v15, v4
	v_and_b32_e32 v4, 0xffff0000, v8
	v_fmac_f32_e32 v38, v15, v4
	v_lshlrev_b32_e32 v4, 16, v9
	v_fmac_f32_e32 v39, v15, v4
	v_and_b32_e32 v4, 0xffff0000, v9
	v_fmac_f32_e32 v40, v15, v4
	v_lshlrev_b32_e32 v4, 16, v10
	v_fmac_f32_e32 v41, v15, v4
	v_and_b32_e32 v4, 0xffff0000, v10
	v_fmac_f32_e32 v42, v15, v4
	v_lshlrev_b32_e32 v4, 16, v11
	v_fmac_f32_e32 v43, v15, v4
	v_sub_f32_e32 v4, v33, v36
	v_mul_f32_e32 v4, 0x3e38aa3b, v4
	v_exp_f32_e32 v12, v4
	ds_read_b128 v[4:7], v14 offset:49152
	v_and_b32_e32 v8, 0xffff0000, v11
	v_fmac_f32_e32 v37, v15, v8
	ds_read_b128 v[8:11], v14 offset:57344
	v_fmac_f32_e32 v13, v32, v15
	s_waitcnt lgkmcnt(1)
	v_lshlrev_b32_e32 v14, 16, v4
	v_and_b32_e32 v4, 0xffff0000, v4
	v_fmac_f32_e32 v38, v12, v4
	v_lshlrev_b32_e32 v4, 16, v5
	v_fmac_f32_e32 v39, v12, v4
	v_and_b32_e32 v4, 0xffff0000, v5
	v_sub_f32_e32 v5, v28, v36
	v_fmac_f32_e32 v40, v12, v4
	v_lshlrev_b32_e32 v4, 16, v6
	v_mul_f32_e32 v5, 0x3e38aa3b, v5
	v_fmac_f32_e32 v41, v12, v4
	v_and_b32_e32 v4, 0xffff0000, v6
	v_exp_f32_e32 v5, v5
	v_fmac_f32_e32 v42, v12, v4
	v_lshlrev_b32_e32 v4, 16, v7
	v_fmac_f32_e32 v43, v12, v4
	v_and_b32_e32 v4, 0xffff0000, v7
	v_fmac_f32_e32 v16, v12, v14
	v_fmac_f32_e32 v37, v12, v4
	s_waitcnt lgkmcnt(0)
	v_lshlrev_b32_e32 v4, 16, v8
	v_fmac_f32_e32 v16, v5, v4
	v_and_b32_e32 v4, 0xffff0000, v8
	v_fmac_f32_e32 v38, v5, v4
	v_lshlrev_b32_e32 v4, 16, v9
	v_fmac_f32_e32 v13, v34, v12
	v_fmac_f32_e32 v39, v5, v4
	v_and_b32_e32 v4, 0xffff0000, v9
	v_fmac_f32_e32 v13, v35, v5
	v_fmac_f32_e32 v40, v5, v4
	v_lshlrev_b32_e32 v4, 16, v10
	v_fmac_f32_e32 v41, v5, v4
	v_and_b32_e32 v4, 0xffff0000, v10
	v_rcp_f32_e32 v6, v13
	v_fmac_f32_e32 v42, v5, v4
	v_lshlrev_b32_e32 v4, 16, v11
	v_fmac_f32_e32 v43, v5, v4
	v_and_b32_e32 v4, 0xffff0000, v11
	v_fmac_f32_e32 v37, v5, v4
	s_waitcnt vmcnt(38)
	v_fmac_f32_e32 v111, v6, v38
	s_waitcnt vmcnt(37)
	v_fmac_f32_e32 v112, v6, v39
	global_store_dword v118, v111, s[80:81] offset:-4096 nt
	global_store_dword v118, v112, s[80:81] nt
	s_waitcnt vmcnt(34)
	v_fmac_f32_e32 v117, v6, v40
	global_store_dword v118, v117, s[82:83] nt
	v_fmac_f32_e32 v113, v6, v41
	global_store_dword v118, v113, s[84:85] offset:-4096 nt
	v_fmac_f32_e32 v114, v6, v42
	global_store_dword v118, v114, s[84:85] nt
	v_fmac_f32_e32 v110, v6, v16
	global_store_dword v118, v110, s[14:15] nt
	v_fmac_f32_e32 v115, v6, v43
	v_fmac_f32_e32 v116, v6, v37
	s_and_b64 vcc, exec, s[18:19]
	global_store_dword v118, v115, s[86:87] offset:-4096 nt
	global_store_dword v118, v116, s[86:87] nt
	s_barrier
	s_cbranch_vccnz .LBB3_144
.LBB3_142:
	s_lshl_b32 s2, s41, 5
	s_add_i32 s2, s2, s22
	s_xor_b64 s[18:19], s[20:21], -1
	s_lshr_b32 s20, s2, 3
	v_mov_b32_e32 v210, v0
	s_add_i32 s20, s20, s24
	s_add_i32 s2, s20, s25
	v_ashrrev_i32_e32 v212, 6, v210
	v_lshl_add_u32 v2, s2, 3, v212
	v_ashrrev_i32_e32 v3, 31, v2
	v_and_b32_e32 v213, 63, v210
	v_lshlrev_b64 v[2:3], 15, v[2:3]
	v_lshl_add_u64 v[2:3], s[10:11], 0, v[2:3]
	v_lshlrev_b32_e32 v206, 4, v213
	v_lshl_add_u64 v[204:205], v[2:3], 0, v[206:207]
	v_and_b32_e32 v2, 3, v212
	v_lshlrev_b32_e32 v3, 3, v212
	v_and_or_b32 v214, v3, 32, v2
	v_and_b32_e32 v2, 0x3fffff8, v212
	v_add_u32_e32 v4, 8, v212
	v_or_b32_e32 v2, s23, v2
	v_and_b32_e32 v4, 0x3fffff8, v4
	v_or_b32_e32 v6, 8, v214
	v_lshlrev_b32_e32 v215, 6, v2
	v_or_b32_e32 v4, s23, v4
	v_or_b32_e32 v2, v6, v215
	v_lshlrev_b32_e32 v216, 6, v4
	v_lshlrev_b32_e32 v209, 10, v212
	v_ashrrev_i32_e32 v3, 31, v2
	v_or_b32_e32 v4, v216, v6
	v_or_b32_e32 v208, v206, v209
	v_lshl_add_u64 v[202:203], s[0:1], 0, v[206:207]
	v_lshlrev_b64 v[2:3], 10, v[2:3]
	v_ashrrev_i32_e32 v5, 31, v4
	s_waitcnt vmcnt(17)
	ds_write_b128 v208, v[190:193]
	s_waitcnt vmcnt(16)
	ds_write_b128 v208, v[194:197] offset:8192
	s_waitcnt vmcnt(15)
	ds_write_b128 v208, v[198:201] offset:16384
	v_lshl_add_u64 v[2:3], v[202:203], 0, v[2:3]
	v_lshlrev_b64 v[4:5], 10, v[4:5]
	v_lshl_add_u64 v[4:5], v[202:203], 0, v[4:5]
	global_load_dwordx4 v[98:101], v[2:3], off
	global_load_dwordx4 v[102:105], v[4:5], off
	v_add_u32_e32 v2, 16, v212
	v_and_b32_e32 v2, 0x3fffff8, v2
	v_or_b32_e32 v2, s23, v2
	v_lshlrev_b32_e32 v217, 6, v2
	v_or_b32_e32 v2, v217, v6
	v_ashrrev_i32_e32 v3, 31, v2
	v_lshlrev_b64 v[2:3], 10, v[2:3]
	v_lshl_add_u64 v[2:3], v[202:203], 0, v[2:3]
	global_load_dwordx4 v[106:109], v[2:3], off
	v_lshrrev_b32_e32 v2, 3, v210
	v_or_b32_e32 v10, 12, v214
	v_and_b32_e32 v211, 4, v2
	v_or_b32_e32 v2, v10, v215
	v_ashrrev_i32_e32 v3, 31, v2
	v_or_b32_e32 v4, v10, v216
	v_lshlrev_b64 v[2:3], 10, v[2:3]
	v_ashrrev_i32_e32 v5, 31, v4
	v_lshl_add_u64 v[2:3], v[202:203], 0, v[2:3]
	v_lshlrev_b64 v[4:5], 10, v[4:5]
	s_waitcnt lgkmcnt(0)
	s_barrier
	v_lshl_add_u64 v[4:5], v[202:203], 0, v[4:5]
	global_load_dwordx4 v[118:121], v[2:3], off
	global_load_dwordx4 v[122:125], v[4:5], off
	v_or_b32_e32 v2, v10, v217
	v_ashrrev_i32_e32 v3, 31, v2
	v_lshlrev_b64 v[2:3], 10, v[2:3]
	v_lshl_add_u64 v[2:3], v[202:203], 0, v[2:3]
	global_load_dwordx4 v[190:193], v[2:3], off
	v_lshlrev_b32_e32 v7, 2, v211
	v_or_b32_e32 v8, 0x1e000, v7
	v_or_b32_e32 v2, 0x1e040, v7
	v_or_b32_e32 v9, 0x1e020, v7
	ds_read_b128 v[50:53], v8
	ds_read_b128 v[54:57], v9
	v_or_b32_e32 v3, 0x1e060, v7
	ds_read_b128 v[58:61], v2
	ds_read_b128 v[62:65], v3
	v_or_b32_e32 v2, 0x1e080, v7
	v_or_b32_e32 v3, 0x1e0a0, v7
	ds_read_b128 v[18:21], v2
	ds_read_b128 v[22:25], v3
	v_or_b32_e32 v2, 0x1e0c0, v7
	v_or_b32_e32 v3, 0x1e0e0, v7
	ds_read_b128 v[26:29], v2
	ds_read_b128 v[30:33], v3
	v_or_b32_e32 v2, 0x1e100, v7
	v_and_b32_e32 v1, 31, v210
	v_or_b32_e32 v3, 0x1e120, v7
	ds_read_b128 v[82:85], v2
	ds_read_b128 v[86:89], v3
	v_or_b32_e32 v2, 0x1e140, v7
	v_lshlrev_b32_e32 v6, 2, v1
	v_or_b32_e32 v3, 0x1e160, v7
	ds_read_b128 v[90:93], v2
	ds_read_b128 v[94:97], v3
	v_or_b32_e32 v2, 0x1e180, v7
	v_or_b32_e32 v3, 0x1e1a0, v7
	ds_read_b128 v[34:37], v2
	ds_read_b128 v[38:41], v3
	v_or_b32_e32 v2, 0x1e1c0, v7
	v_or_b32_e32 v4, 0x1e200, v6
	v_or_b32_e32 v3, 0x1e1e0, v7
	ds_read_b32 v66, v4
	ds_read_b128 v[42:45], v2
	ds_read_b128 v[46:49], v3
	v_or_b32_e32 v2, 0x1e280, v6
	ds_read_b32 v2, v2
	ds_read_b128 v[110:113], v206
	ds_read_b128 v[114:117], v206 offset:4096
	ds_read_b128 v[126:129], v206 offset:8192
	ds_read_b128 v[194:197], v206 offset:12288
	ds_read_b128 v[198:201], v206 offset:16384
	ds_read_b128 v[218:221], v206 offset:20480
	s_waitcnt vmcnt(20)
	ds_write_b128 v208, v[174:177] offset:24576
	s_waitcnt vmcnt(19)
	ds_write_b128 v208, v[182:185] offset:32768
	s_waitcnt vmcnt(18)
	ds_write_b128 v208, v[186:189] offset:40960
	ds_read_b128 v[174:177], v206 offset:1024
	ds_read_b128 v[182:185], v206 offset:5120
	ds_read_b128 v[186:189], v206 offset:9216
	ds_read_b128 v[222:225], v206 offset:13312
	ds_read_b128 v[226:229], v206 offset:17408
	ds_read_b128 v[230:233], v206 offset:21504
	s_waitcnt lgkmcnt(14)
	v_mov_b32_e32 v67, v66
	v_mov_b32_e32 v68, v66
	v_mov_b32_e32 v69, v66
	v_mov_b32_e32 v70, v66
	v_mov_b32_e32 v71, v66
	v_mov_b32_e32 v72, v66
	v_mov_b32_e32 v73, v66
	v_mov_b32_e32 v74, v66
	v_mov_b32_e32 v75, v66
	v_mov_b32_e32 v76, v66
	v_mov_b32_e32 v77, v66
	v_mov_b32_e32 v78, v66
	v_mov_b32_e32 v79, v66
	v_mov_b32_e32 v80, v66
	v_mov_b32_e32 v81, v66
	v_mov_b32_e32 v3, v2
	v_mov_b32_e32 v4, v2
	v_mov_b32_e32 v5, v2
	v_mov_b32_e32 v6, v2
	v_mov_b32_e32 v7, v2
	v_mov_b32_e32 v8, v2
	v_mov_b32_e32 v9, v2
	v_mov_b32_e32 v10, v2
	v_mov_b32_e32 v11, v2
	v_mov_b32_e32 v12, v2
	v_mov_b32_e32 v13, v2
	v_mov_b32_e32 v14, v2
	v_mov_b32_e32 v15, v2
	v_mov_b32_e32 v16, v2
	v_mov_b32_e32 v17, v2
	s_waitcnt vmcnt(17)
	v_mfma_f32_32x32x16_bf16 v[50:65], v[110:113], v[170:173], v[50:65]
	s_waitcnt lgkmcnt(13)
	v_mfma_f32_32x32x16_bf16 v[18:33], v[114:117], v[170:173], v[18:33]
	s_waitcnt lgkmcnt(12)
	v_mfma_f32_32x32x16_bf16 v[82:97], v[126:129], v[170:173], v[82:97]
	s_waitcnt lgkmcnt(11)
	v_mfma_f32_32x32x16_bf16 v[34:49], v[194:197], v[170:173], v[34:49]
	s_waitcnt lgkmcnt(10)
	v_mfma_f32_32x32x16_bf16 v[66:81], v[170:173], v[198:201], v[66:81]
	s_waitcnt lgkmcnt(9)
	v_mfma_f32_32x32x16_bf16 v[2:17], v[170:173], v[218:221], v[2:17]
	ds_read_b128 v[110:113], v206 offset:2048
	ds_read_b128 v[114:117], v206 offset:6144
	ds_read_b128 v[126:129], v206 offset:10240
	ds_read_b128 v[170:173], v206 offset:14336
	ds_read_b128 v[194:197], v206 offset:18432
	ds_read_b128 v[198:201], v206 offset:22528
	s_waitcnt vmcnt(16) lgkmcnt(11)
	v_mfma_f32_32x32x16_bf16 v[50:65], v[174:177], v[162:165], v[50:65]
	s_waitcnt lgkmcnt(10)
	v_mfma_f32_32x32x16_bf16 v[18:33], v[182:185], v[162:165], v[18:33]
	s_waitcnt lgkmcnt(9)
	v_mfma_f32_32x32x16_bf16 v[82:97], v[186:189], v[162:165], v[82:97]
	s_waitcnt lgkmcnt(8)
	v_mfma_f32_32x32x16_bf16 v[34:49], v[222:225], v[162:165], v[34:49]
	s_waitcnt lgkmcnt(7)
	v_mfma_f32_32x32x16_bf16 v[66:81], v[162:165], v[226:229], v[66:81]
	s_waitcnt lgkmcnt(6)
	v_mfma_f32_32x32x16_bf16 v[2:17], v[162:165], v[230:233], v[2:17]
	s_waitcnt lgkmcnt(6)
	s_barrier
	ds_read_b128 v[162:165], v206 offset:3072
	ds_read_b128 v[174:177], v206 offset:7168
	ds_read_b128 v[182:185], v206 offset:11264
	ds_read_b128 v[186:189], v206 offset:15360
	ds_read_b128 v[218:221], v206 offset:19456
	ds_read_b128 v[222:225], v206 offset:23552
	s_waitcnt vmcnt(15) lgkmcnt(11)
	v_mfma_f32_32x32x16_bf16 v[50:65], v[110:113], v[154:157], v[50:65]
	s_waitcnt lgkmcnt(10)
	v_mfma_f32_32x32x16_bf16 v[18:33], v[114:117], v[154:157], v[18:33]
	s_waitcnt lgkmcnt(9)
	v_mfma_f32_32x32x16_bf16 v[82:97], v[126:129], v[154:157], v[82:97]
	s_waitcnt lgkmcnt(8)
	v_mfma_f32_32x32x16_bf16 v[34:49], v[170:173], v[154:157], v[34:49]
	s_waitcnt lgkmcnt(7)
	v_mfma_f32_32x32x16_bf16 v[66:81], v[154:157], v[194:197], v[66:81]
	s_waitcnt lgkmcnt(6)
	v_mfma_f32_32x32x16_bf16 v[2:17], v[154:157], v[198:201], v[2:17]
	ds_read_b128 v[194:197], v206 offset:24576
	ds_read_b128 v[198:201], v206 offset:28672
	ds_read_b128 v[226:229], v206 offset:32768
	ds_read_b128 v[230:233], v206 offset:36864
	ds_read_b128 v[234:237], v206 offset:40960
	ds_read_b128 v[238:241], v206 offset:45056
	v_add_co_u32_e32 v110, vcc, s29, v204
	s_waitcnt vmcnt(14) lgkmcnt(11)
	v_mfma_f32_32x32x16_bf16 v[50:65], v[162:165], v[146:149], v[50:65]
	v_addc_co_u32_e32 v111, vcc, 0, v205, vcc
	v_add_co_u32_e32 v242, vcc, s30, v204
	s_nop 1
	v_addc_co_u32_e32 v243, vcc, 0, v205, vcc
	global_load_dwordx4 v[126:129], v[110:111], off offset:1024
	global_load_dwordx4 v[114:117], v[110:111], off offset:2048
	global_load_dwordx4 v[154:157], v[242:243], off offset:-4096
	s_nop 0
	global_load_dwordx4 v[110:113], v[110:111], off offset:3072
	s_waitcnt lgkmcnt(10)
	v_mfma_f32_32x32x16_bf16 v[18:33], v[174:177], v[146:149], v[18:33]
	s_waitcnt lgkmcnt(9)
	v_mfma_f32_32x32x16_bf16 v[82:97], v[182:185], v[146:149], v[82:97]
	s_waitcnt lgkmcnt(8)
	v_mfma_f32_32x32x16_bf16 v[34:49], v[186:189], v[146:149], v[34:49]
	s_waitcnt lgkmcnt(7)
	v_mfma_f32_32x32x16_bf16 v[66:81], v[146:149], v[218:221], v[66:81]
	s_waitcnt lgkmcnt(6)
	v_mfma_f32_32x32x16_bf16 v[2:17], v[146:149], v[222:225], v[2:17]
	v_or_b32_e32 v170, 16, v214
	v_or_b32_e32 v146, v170, v215
	v_or_b32_e32 v148, v170, v216
	v_or_b32_e32 v170, v170, v217
	v_ashrrev_i32_e32 v147, 31, v146
	v_ashrrev_i32_e32 v149, 31, v148
	v_ashrrev_i32_e32 v171, 31, v170
	v_lshlrev_b64 v[146:147], 10, v[146:147]
	v_lshlrev_b64 v[148:149], 10, v[148:149]
	v_lshlrev_b64 v[170:171], 10, v[170:171]
	v_lshl_add_u64 v[146:147], v[202:203], 0, v[146:147]
	v_lshl_add_u64 v[162:163], v[202:203], 0, v[148:149]
	v_lshl_add_u64 v[170:171], v[202:203], 0, v[170:171]
	global_load_dwordx4 v[146:149], v[146:147], off
	s_nop 0
	global_load_dwordx4 v[162:165], v[162:163], off
	v_or_b32_e32 v244, 0x10000, v206
	global_load_dwordx4 v[170:173], v[170:171], off
	v_add_u32_e32 v209, v244, v209
	s_waitcnt vmcnt(12)
	ds_write_b128 v208, v[98:101] offset:49152
	s_waitcnt vmcnt(11)
	ds_write_b128 v208, v[102:105] offset:57344
	s_waitcnt vmcnt(10)
	ds_write_b128 v209, v[106:109]
	ds_read_b128 v[98:101], v206 offset:25600
	ds_read_b128 v[102:105], v206 offset:29696
	ds_read_b128 v[106:109], v206 offset:33792
	ds_read_b128 v[174:177], v206 offset:37888
	ds_read_b128 v[182:185], v206 offset:41984
	ds_read_b128 v[186:189], v206 offset:46080
	s_waitcnt lgkmcnt(14)
	v_mfma_f32_32x32x16_bf16 v[50:65], v[194:197], v[178:181], v[50:65]
	s_waitcnt lgkmcnt(13)
	v_mfma_f32_32x32x16_bf16 v[18:33], v[198:201], v[178:181], v[18:33]
	s_waitcnt lgkmcnt(12)
	v_mfma_f32_32x32x16_bf16 v[82:97], v[226:229], v[178:181], v[82:97]
	s_waitcnt lgkmcnt(11)
	v_mfma_f32_32x32x16_bf16 v[34:49], v[230:233], v[178:181], v[34:49]
	s_waitcnt lgkmcnt(10)
	v_mfma_f32_32x32x16_bf16 v[66:81], v[178:181], v[234:237], v[66:81]
	s_waitcnt lgkmcnt(9)
	v_mfma_f32_32x32x16_bf16 v[2:17], v[178:181], v[238:241], v[2:17]
	ds_read_b128 v[178:181], v206 offset:26624
	ds_read_b128 v[194:197], v206 offset:30720
	ds_read_b128 v[198:201], v206 offset:34816
	ds_read_b128 v[218:221], v206 offset:38912
	ds_read_b128 v[222:225], v206 offset:43008
	ds_read_b128 v[226:229], v206 offset:47104
	s_waitcnt lgkmcnt(11)
	v_mfma_f32_32x32x16_bf16 v[50:65], v[98:101], v[166:169], v[50:65]
	s_waitcnt lgkmcnt(10)
	v_mfma_f32_32x32x16_bf16 v[18:33], v[102:105], v[166:169], v[18:33]
	s_waitcnt lgkmcnt(9)
	v_mfma_f32_32x32x16_bf16 v[82:97], v[106:109], v[166:169], v[82:97]
	s_waitcnt lgkmcnt(8)
	v_mfma_f32_32x32x16_bf16 v[34:49], v[174:177], v[166:169], v[34:49]
	s_waitcnt lgkmcnt(7)
	v_mfma_f32_32x32x16_bf16 v[66:81], v[166:169], v[182:185], v[66:81]
	s_waitcnt lgkmcnt(6)
	v_mfma_f32_32x32x16_bf16 v[2:17], v[166:169], v[186:189], v[2:17]
	s_waitcnt lgkmcnt(6)
	s_barrier
	ds_read_b128 v[98:101], v206 offset:27648
	ds_read_b128 v[102:105], v206 offset:31744
	ds_read_b128 v[106:109], v206 offset:35840
	ds_read_b128 v[166:169], v206 offset:39936
	ds_read_b128 v[174:177], v206 offset:44032
	ds_read_b128 v[182:185], v206 offset:48128
	s_waitcnt lgkmcnt(11)
	v_mfma_f32_32x32x16_bf16 v[50:65], v[178:181], v[158:161], v[50:65]
	s_waitcnt lgkmcnt(10)
	v_mfma_f32_32x32x16_bf16 v[18:33], v[194:197], v[158:161], v[18:33]
	s_waitcnt lgkmcnt(9)
	v_mfma_f32_32x32x16_bf16 v[82:97], v[198:201], v[158:161], v[82:97]
	s_waitcnt lgkmcnt(8)
	v_mfma_f32_32x32x16_bf16 v[34:49], v[218:221], v[158:161], v[34:49]
	s_waitcnt lgkmcnt(7)
	v_mfma_f32_32x32x16_bf16 v[66:81], v[158:161], v[222:225], v[66:81]
	s_waitcnt lgkmcnt(6)
	v_mfma_f32_32x32x16_bf16 v[2:17], v[158:161], v[226:229], v[2:17]
	ds_read_b128 v[186:189], v206 offset:49152
	ds_read_b128 v[194:197], v206 offset:53248
	ds_read_b128 v[198:201], v206 offset:57344
	ds_read_b128 v[218:221], v206 offset:61440
	v_or_b32_e32 v240, 0x11000, v206
	ds_read_b128 v[222:225], v244
	ds_read_b128 v[226:229], v240
	s_waitcnt lgkmcnt(11)
	v_mfma_f32_32x32x16_bf16 v[50:65], v[98:101], v[150:153], v[50:65]
	s_waitcnt lgkmcnt(10)
	v_mfma_f32_32x32x16_bf16 v[18:33], v[102:105], v[150:153], v[18:33]
	s_waitcnt lgkmcnt(9)
	v_mfma_f32_32x32x16_bf16 v[82:97], v[106:109], v[150:153], v[82:97]
	global_load_dwordx4 v[158:161], v[242:243], off
	global_load_dwordx4 v[106:109], v[242:243], off offset:1024
	global_load_dwordx4 v[102:105], v[242:243], off offset:2048
	global_load_dwordx4 v[98:101], v[242:243], off offset:3072
	s_waitcnt lgkmcnt(8)
	v_mfma_f32_32x32x16_bf16 v[34:49], v[166:169], v[150:153], v[34:49]
	s_waitcnt lgkmcnt(7)
	v_mfma_f32_32x32x16_bf16 v[66:81], v[150:153], v[174:177], v[66:81]
	s_waitcnt lgkmcnt(6)
	v_mfma_f32_32x32x16_bf16 v[2:17], v[150:153], v[182:185], v[2:17]
	v_or_b32_e32 v174, 20, v214
	v_or_b32_e32 v150, v174, v215
	v_or_b32_e32 v152, v174, v216
	v_or_b32_e32 v174, v174, v217
	v_ashrrev_i32_e32 v151, 31, v150
	v_ashrrev_i32_e32 v153, 31, v152
	v_ashrrev_i32_e32 v175, 31, v174
	v_lshlrev_b64 v[150:151], 10, v[150:151]
	v_lshlrev_b64 v[152:153], 10, v[152:153]
	v_lshlrev_b64 v[174:175], 10, v[174:175]
	v_lshl_add_u64 v[150:151], v[202:203], 0, v[150:151]
	v_lshl_add_u64 v[166:167], v[202:203], 0, v[152:153]
	v_lshl_add_u64 v[174:175], v[202:203], 0, v[174:175]
	global_load_dwordx4 v[150:153], v[150:151], off
	s_nop 0
	global_load_dwordx4 v[166:169], v[166:167], off
	v_or_b32_e32 v241, 0x10400, v206
	global_load_dwordx4 v[178:181], v[174:175], off
	s_waitcnt vmcnt(16)
	ds_write_b128 v208, v[118:121]
	s_waitcnt vmcnt(15)
	ds_write_b128 v208, v[122:125] offset:8192
	s_waitcnt vmcnt(14)
	ds_write_b128 v208, v[190:193] offset:16384
	ds_read_b128 v[118:121], v206 offset:50176
	ds_read_b128 v[122:125], v206 offset:54272
	ds_read_b128 v[174:177], v206 offset:58368
	ds_read_b128 v[182:185], v206 offset:62464
	v_or_b32_e32 v242, 0x11400, v206
	ds_read_b128 v[190:193], v241
	ds_read_b128 v[230:233], v242
	s_waitcnt lgkmcnt(14)
	v_mfma_f32_32x32x16_bf16 v[50:65], v[186:189], v[142:145], v[50:65]
	s_waitcnt lgkmcnt(13)
	v_mfma_f32_32x32x16_bf16 v[18:33], v[194:197], v[142:145], v[18:33]
	s_waitcnt lgkmcnt(12)
	v_mfma_f32_32x32x16_bf16 v[82:97], v[198:201], v[142:145], v[82:97]
	s_waitcnt lgkmcnt(11)
	v_mfma_f32_32x32x16_bf16 v[34:49], v[218:221], v[142:145], v[34:49]
	s_waitcnt lgkmcnt(10)
	v_mfma_f32_32x32x16_bf16 v[66:81], v[142:145], v[222:225], v[66:81]
	s_waitcnt lgkmcnt(9)
	v_mfma_f32_32x32x16_bf16 v[2:17], v[142:145], v[226:229], v[2:17]
	ds_read_b128 v[142:145], v206 offset:51200
	ds_read_b128 v[186:189], v206 offset:55296
	ds_read_b128 v[194:197], v206 offset:59392
	ds_read_b128 v[198:201], v206 offset:63488
	v_or_b32_e32 v243, 0x10800, v206
	v_or_b32_e32 v245, 0x11800, v206
	ds_read_b128 v[218:221], v243
	ds_read_b128 v[222:225], v245
	s_waitcnt lgkmcnt(11)
	v_mfma_f32_32x32x16_bf16 v[50:65], v[118:121], v[138:141], v[50:65]
	s_waitcnt lgkmcnt(10)
	v_mfma_f32_32x32x16_bf16 v[18:33], v[122:125], v[138:141], v[18:33]
	s_waitcnt lgkmcnt(9)
	v_mfma_f32_32x32x16_bf16 v[82:97], v[174:177], v[138:141], v[82:97]
	s_waitcnt lgkmcnt(8)
	v_mfma_f32_32x32x16_bf16 v[34:49], v[182:185], v[138:141], v[34:49]
	s_waitcnt lgkmcnt(7)
	v_mfma_f32_32x32x16_bf16 v[66:81], v[138:141], v[190:193], v[66:81]
	s_waitcnt lgkmcnt(6)
	v_mfma_f32_32x32x16_bf16 v[2:17], v[138:141], v[230:233], v[2:17]
	s_waitcnt lgkmcnt(6)
	s_barrier
	ds_read_b128 v[118:121], v206 offset:52224
	ds_read_b128 v[122:125], v206 offset:56320
	ds_read_b128 v[138:141], v206 offset:60416
	ds_read_b128 v[174:177], v206 offset:64512
	v_or_b32_e32 v246, 0x10c00, v206
	v_or_b32_e32 v247, 0x11c00, v206
	ds_read_b128 v[182:185], v246
	ds_read_b128 v[190:193], v247
	s_waitcnt lgkmcnt(11)
	v_mfma_f32_32x32x16_bf16 v[50:65], v[142:145], v[134:137], v[50:65]
	s_waitcnt lgkmcnt(10)
	v_mfma_f32_32x32x16_bf16 v[18:33], v[186:189], v[134:137], v[18:33]
	s_waitcnt lgkmcnt(9)
	v_mfma_f32_32x32x16_bf16 v[82:97], v[194:197], v[134:137], v[82:97]
	s_waitcnt lgkmcnt(8)
	v_mfma_f32_32x32x16_bf16 v[34:49], v[198:201], v[134:137], v[34:49]
	s_waitcnt lgkmcnt(7)
	v_mfma_f32_32x32x16_bf16 v[66:81], v[134:137], v[218:221], v[66:81]
	s_waitcnt lgkmcnt(6)
	v_mfma_f32_32x32x16_bf16 v[2:17], v[134:137], v[222:225], v[2:17]
	ds_read_b128 v[186:189], v206
	ds_read_b128 v[218:221], v206 offset:4096
	ds_read_b128 v[222:225], v206 offset:8192
	ds_read_b128 v[226:229], v206 offset:12288
	ds_read_b128 v[230:233], v206 offset:16384
	ds_read_b128 v[234:237], v206 offset:20480
	s_waitcnt lgkmcnt(11)
	v_mfma_f32_32x32x16_bf16 v[50:65], v[118:121], v[130:133], v[50:65]
	v_add_co_u32_e32 v118, vcc, s31, v204
	s_nop 1
	v_addc_co_u32_e32 v119, vcc, 0, v205, vcc
	v_add_co_u32_e32 v238, vcc, s27, v204
	s_waitcnt lgkmcnt(10)
	v_mfma_f32_32x32x16_bf16 v[18:33], v[122:125], v[130:133], v[18:33]
	v_addc_co_u32_e32 v239, vcc, 0, v205, vcc
	s_waitcnt lgkmcnt(9)
	v_mfma_f32_32x32x16_bf16 v[82:97], v[138:141], v[130:133], v[82:97]
	global_load_dwordx4 v[138:141], v[118:119], off offset:1024
	global_load_dwordx4 v[134:137], v[118:119], off offset:2048
	s_waitcnt lgkmcnt(8)
	v_mfma_f32_32x32x16_bf16 v[34:49], v[174:177], v[130:133], v[34:49]
	s_waitcnt lgkmcnt(7)
	v_mfma_f32_32x32x16_bf16 v[66:81], v[130:133], v[182:185], v[66:81]
	s_waitcnt lgkmcnt(6)
	v_mfma_f32_32x32x16_bf16 v[2:17], v[130:133], v[190:193], v[2:17]
	global_load_dwordx4 v[142:145], v[238:239], off offset:-4096
	global_load_dwordx4 v[130:133], v[118:119], off offset:3072
	v_or_b32_e32 v122, 24, v214
	v_or_b32_e32 v118, v122, v215
	v_ashrrev_i32_e32 v119, 31, v118
	v_or_b32_e32 v120, v122, v216
	v_lshlrev_b64 v[118:119], 10, v[118:119]
	v_ashrrev_i32_e32 v121, 31, v120
	v_lshl_add_u64 v[118:119], v[202:203], 0, v[118:119]
	v_lshlrev_b64 v[120:121], 10, v[120:121]
	v_lshl_add_u64 v[120:121], v[202:203], 0, v[120:121]
	global_load_dwordx4 v[190:193], v[118:119], off
	global_load_dwordx4 v[194:197], v[120:121], off
	v_or_b32_e32 v118, v122, v217
	v_ashrrev_i32_e32 v119, 31, v118
	v_lshlrev_b64 v[118:119], 10, v[118:119]
	v_lshl_add_u64 v[118:119], v[202:203], 0, v[118:119]
	global_load_dwordx4 v[198:201], v[118:119], off
	s_waitcnt vmcnt(16)
	ds_write_b128 v208, v[146:149] offset:24576
	s_waitcnt vmcnt(15)
	ds_write_b128 v208, v[162:165] offset:32768
	s_waitcnt vmcnt(14)
	ds_write_b128 v208, v[170:173] offset:40960
	ds_read_b128 v[118:121], v206 offset:1024
	ds_read_b128 v[122:125], v206 offset:5120
	ds_read_b128 v[146:149], v206 offset:9216
	ds_read_b128 v[162:165], v206 offset:13312
	ds_read_b128 v[170:173], v206 offset:17408
	ds_read_b128 v[174:177], v206 offset:21504
	s_waitcnt lgkmcnt(14)
	v_mfma_f32_32x32x16_bf16 v[50:65], v[186:189], v[154:157], v[50:65]
	s_waitcnt lgkmcnt(13)
	v_mfma_f32_32x32x16_bf16 v[18:33], v[218:221], v[154:157], v[18:33]
	s_waitcnt lgkmcnt(12)
	v_mfma_f32_32x32x16_bf16 v[82:97], v[222:225], v[154:157], v[82:97]
	s_waitcnt lgkmcnt(11)
	v_mfma_f32_32x32x16_bf16 v[34:49], v[226:229], v[154:157], v[34:49]
	s_waitcnt lgkmcnt(10)
	v_mfma_f32_32x32x16_bf16 v[66:81], v[154:157], v[230:233], v[66:81]
	s_waitcnt lgkmcnt(9)
	v_mfma_f32_32x32x16_bf16 v[2:17], v[154:157], v[234:237], v[2:17]
	ds_read_b128 v[154:157], v206 offset:2048
	ds_read_b128 v[182:185], v206 offset:6144
	ds_read_b128 v[186:189], v206 offset:10240
	ds_read_b128 v[218:221], v206 offset:14336
	ds_read_b128 v[222:225], v206 offset:18432
	ds_read_b128 v[226:229], v206 offset:22528
	s_waitcnt lgkmcnt(11)
	v_mfma_f32_32x32x16_bf16 v[50:65], v[118:121], v[126:129], v[50:65]
	s_waitcnt lgkmcnt(10)
	v_mfma_f32_32x32x16_bf16 v[18:33], v[122:125], v[126:129], v[18:33]
	s_waitcnt lgkmcnt(9)
	v_mfma_f32_32x32x16_bf16 v[82:97], v[146:149], v[126:129], v[82:97]
	s_waitcnt lgkmcnt(8)
	v_mfma_f32_32x32x16_bf16 v[34:49], v[162:165], v[126:129], v[34:49]
	s_waitcnt lgkmcnt(7)
	v_mfma_f32_32x32x16_bf16 v[66:81], v[126:129], v[170:173], v[66:81]
	s_waitcnt lgkmcnt(6)
	v_mfma_f32_32x32x16_bf16 v[2:17], v[126:129], v[174:177], v[2:17]
	s_waitcnt lgkmcnt(6)
	s_barrier
	ds_read_b128 v[118:121], v206 offset:3072
	ds_read_b128 v[122:125], v206 offset:7168
	ds_read_b128 v[126:129], v206 offset:11264
	ds_read_b128 v[146:149], v206 offset:15360
	ds_read_b128 v[162:165], v206 offset:19456
	ds_read_b128 v[174:177], v206 offset:23552
	s_waitcnt lgkmcnt(11)
	v_mfma_f32_32x32x16_bf16 v[50:65], v[154:157], v[114:117], v[50:65]
	s_waitcnt lgkmcnt(10)
	v_mfma_f32_32x32x16_bf16 v[18:33], v[182:185], v[114:117], v[18:33]
	s_waitcnt lgkmcnt(9)
	v_mfma_f32_32x32x16_bf16 v[82:97], v[186:189], v[114:117], v[82:97]
	s_waitcnt lgkmcnt(8)
	v_mfma_f32_32x32x16_bf16 v[34:49], v[218:221], v[114:117], v[34:49]
	s_waitcnt lgkmcnt(7)
	v_mfma_f32_32x32x16_bf16 v[66:81], v[114:117], v[222:225], v[66:81]
	s_waitcnt lgkmcnt(6)
	v_mfma_f32_32x32x16_bf16 v[2:17], v[114:117], v[226:229], v[2:17]
	ds_read_b128 v[114:117], v206 offset:24576
	ds_read_b128 v[218:221], v206 offset:28672
	ds_read_b128 v[222:225], v206 offset:32768
	ds_read_b128 v[226:229], v206 offset:36864
	ds_read_b128 v[230:233], v206 offset:40960
	ds_read_b128 v[234:237], v206 offset:45056
	s_waitcnt lgkmcnt(8)
	v_mfma_f32_32x32x16_bf16 v[34:49], v[146:149], v[110:113], v[34:49]
	s_waitcnt lgkmcnt(7)
	v_mfma_f32_32x32x16_bf16 v[66:81], v[110:113], v[162:165], v[66:81]
	global_load_dwordx4 v[170:173], v[238:239], off
	global_load_dwordx4 v[162:165], v[238:239], off offset:1024
	global_load_dwordx4 v[154:157], v[238:239], off offset:2048
	global_load_dwordx4 v[146:149], v[238:239], off offset:3072
	v_mfma_f32_32x32x16_bf16 v[50:65], v[118:121], v[110:113], v[50:65]
	v_mfma_f32_32x32x16_bf16 v[18:33], v[122:125], v[110:113], v[18:33]
	v_mfma_f32_32x32x16_bf16 v[82:97], v[126:129], v[110:113], v[82:97]
	s_waitcnt lgkmcnt(6)
	v_mfma_f32_32x32x16_bf16 v[2:17], v[110:113], v[174:177], v[2:17]
	v_or_b32_e32 v118, 28, v214
	v_or_b32_e32 v110, v118, v215
	v_ashrrev_i32_e32 v111, 31, v110
	v_or_b32_e32 v112, v118, v216
	v_lshlrev_b64 v[110:111], 10, v[110:111]
	v_ashrrev_i32_e32 v113, 31, v112
	v_lshl_add_u64 v[110:111], v[202:203], 0, v[110:111]
	v_lshlrev_b64 v[112:113], 10, v[112:113]
	v_lshl_add_u64 v[112:113], v[202:203], 0, v[112:113]
	global_load_dwordx4 v[174:177], v[110:111], off
	global_load_dwordx4 v[182:185], v[112:113], off
	v_or_b32_e32 v110, v118, v217
	v_ashrrev_i32_e32 v111, 31, v110
	v_lshlrev_b64 v[110:111], 10, v[110:111]
	v_lshl_add_u64 v[110:111], v[202:203], 0, v[110:111]
	global_load_dwordx4 v[186:189], v[110:111], off
	s_waitcnt vmcnt(16)
	ds_write_b128 v208, v[150:153] offset:49152
	s_waitcnt vmcnt(15)
	ds_write_b128 v208, v[166:169] offset:57344
	s_waitcnt vmcnt(14)
	ds_write_b128 v209, v[178:181]
	ds_read_b128 v[110:113], v206 offset:25600
	ds_read_b128 v[118:121], v206 offset:29696
	ds_read_b128 v[122:125], v206 offset:33792
	ds_read_b128 v[126:129], v206 offset:37888
	ds_read_b128 v[150:153], v206 offset:41984
	ds_read_b128 v[166:169], v206 offset:46080
	s_waitcnt lgkmcnt(14)
	v_mfma_f32_32x32x16_bf16 v[50:65], v[114:117], v[158:161], v[50:65]
	s_waitcnt lgkmcnt(13)
	v_mfma_f32_32x32x16_bf16 v[18:33], v[218:221], v[158:161], v[18:33]
	s_waitcnt lgkmcnt(12)
	v_mfma_f32_32x32x16_bf16 v[82:97], v[222:225], v[158:161], v[82:97]
	s_waitcnt lgkmcnt(11)
	v_mfma_f32_32x32x16_bf16 v[34:49], v[226:229], v[158:161], v[34:49]
	s_waitcnt lgkmcnt(10)
	v_mfma_f32_32x32x16_bf16 v[66:81], v[158:161], v[230:233], v[66:81]
	s_waitcnt lgkmcnt(9)
	v_mfma_f32_32x32x16_bf16 v[2:17], v[158:161], v[234:237], v[2:17]
	ds_read_b128 v[114:117], v206 offset:26624
	ds_read_b128 v[158:161], v206 offset:30720
	ds_read_b128 v[178:181], v206 offset:34816
	ds_read_b128 v[218:221], v206 offset:38912
	ds_read_b128 v[222:225], v206 offset:43008
	ds_read_b128 v[226:229], v206 offset:47104
	s_waitcnt lgkmcnt(11)
	v_mfma_f32_32x32x16_bf16 v[50:65], v[110:113], v[106:109], v[50:65]
	s_waitcnt lgkmcnt(10)
	v_mfma_f32_32x32x16_bf16 v[18:33], v[118:121], v[106:109], v[18:33]
	s_waitcnt lgkmcnt(9)
	v_mfma_f32_32x32x16_bf16 v[82:97], v[122:125], v[106:109], v[82:97]
	s_waitcnt lgkmcnt(8)
	v_mfma_f32_32x32x16_bf16 v[34:49], v[126:129], v[106:109], v[34:49]
	s_waitcnt lgkmcnt(7)
	v_mfma_f32_32x32x16_bf16 v[66:81], v[106:109], v[150:153], v[66:81]
	s_waitcnt lgkmcnt(6)
	v_mfma_f32_32x32x16_bf16 v[2:17], v[106:109], v[166:169], v[2:17]
	s_waitcnt lgkmcnt(6)
	s_barrier
	ds_read_b128 v[106:109], v206 offset:27648
	ds_read_b128 v[110:113], v206 offset:31744
	ds_read_b128 v[118:121], v206 offset:35840
	ds_read_b128 v[122:125], v206 offset:39936
	ds_read_b128 v[126:129], v206 offset:44032
	ds_read_b128 v[230:233], v206 offset:48128
	s_waitcnt lgkmcnt(11)
	v_mfma_f32_32x32x16_bf16 v[50:65], v[114:117], v[102:105], v[50:65]
	s_waitcnt lgkmcnt(10)
	v_mfma_f32_32x32x16_bf16 v[18:33], v[158:161], v[102:105], v[18:33]
	s_waitcnt lgkmcnt(9)
	v_mfma_f32_32x32x16_bf16 v[82:97], v[178:181], v[102:105], v[82:97]
	s_waitcnt lgkmcnt(8)
	v_mfma_f32_32x32x16_bf16 v[34:49], v[218:221], v[102:105], v[34:49]
	s_waitcnt lgkmcnt(7)
	v_mfma_f32_32x32x16_bf16 v[66:81], v[102:105], v[222:225], v[66:81]
	s_waitcnt lgkmcnt(6)
	v_mfma_f32_32x32x16_bf16 v[2:17], v[102:105], v[226:229], v[2:17]
	ds_read_b128 v[102:105], v206 offset:49152
	ds_read_b128 v[114:117], v206 offset:53248
	ds_read_b128 v[218:221], v206 offset:57344
	ds_read_b128 v[222:225], v206 offset:61440
	ds_read_b128 v[226:229], v244
	ds_read_b128 v[234:237], v240
	s_waitcnt lgkmcnt(11)
	v_mfma_f32_32x32x16_bf16 v[50:65], v[106:109], v[98:101], v[50:65]
	v_add_co_u32_e32 v106, vcc, s33, v204
	s_nop 1
	v_addc_co_u32_e32 v107, vcc, 0, v205, vcc
	global_load_dwordx4 v[178:181], v[106:107], off
	global_load_dwordx4 v[166:169], v[106:107], off offset:1024
	global_load_dwordx4 v[158:161], v[106:107], off offset:2048
	global_load_dwordx4 v[150:153], v[106:107], off offset:3072
	s_waitcnt lgkmcnt(10)
	v_mfma_f32_32x32x16_bf16 v[18:33], v[110:113], v[98:101], v[18:33]
	s_waitcnt lgkmcnt(9)
	v_mfma_f32_32x32x16_bf16 v[82:97], v[118:121], v[98:101], v[82:97]
	s_waitcnt lgkmcnt(8)
	v_mfma_f32_32x32x16_bf16 v[34:49], v[122:125], v[98:101], v[34:49]
	s_waitcnt lgkmcnt(7)
	v_mfma_f32_32x32x16_bf16 v[66:81], v[98:101], v[126:129], v[66:81]
	s_waitcnt lgkmcnt(6)
	v_mfma_f32_32x32x16_bf16 v[2:17], v[98:101], v[230:233], v[2:17]
	s_waitcnt vmcnt(13)
	ds_write_b128 v208, v[190:193]
	s_waitcnt vmcnt(12)
	ds_write_b128 v208, v[194:197] offset:8192
	s_waitcnt vmcnt(11)
	ds_write_b128 v208, v[198:201] offset:16384
	ds_read_b128 v[98:101], v206 offset:50176
	ds_read_b128 v[106:109], v206 offset:54272
	ds_read_b128 v[110:113], v206 offset:58368
	ds_read_b128 v[118:121], v206 offset:62464
	ds_read_b128 v[122:125], v241
	ds_read_b128 v[126:129], v242
	s_waitcnt lgkmcnt(14)
	v_mfma_f32_32x32x16_bf16 v[50:65], v[102:105], v[142:145], v[50:65]
	s_waitcnt lgkmcnt(13)
	v_mfma_f32_32x32x16_bf16 v[18:33], v[114:117], v[142:145], v[18:33]
	s_waitcnt lgkmcnt(12)
	v_mfma_f32_32x32x16_bf16 v[82:97], v[218:221], v[142:145], v[82:97]
	s_waitcnt lgkmcnt(11)
	v_mfma_f32_32x32x16_bf16 v[34:49], v[222:225], v[142:145], v[34:49]
	s_waitcnt lgkmcnt(10)
	v_mfma_f32_32x32x16_bf16 v[66:81], v[142:145], v[226:229], v[66:81]
	s_waitcnt lgkmcnt(9)
	v_mfma_f32_32x32x16_bf16 v[2:17], v[142:145], v[234:237], v[2:17]
	ds_read_b128 v[102:105], v206 offset:51200
	ds_read_b128 v[114:117], v206 offset:55296
	ds_read_b128 v[218:221], v206 offset:59392
	ds_read_b128 v[222:225], v206 offset:63488
	ds_read_b128 v[226:229], v243
	ds_read_b128 v[230:233], v245
	s_waitcnt lgkmcnt(11)
	v_mfma_f32_32x32x16_bf16 v[50:65], v[98:101], v[138:141], v[50:65]
	s_waitcnt lgkmcnt(10)
	v_mfma_f32_32x32x16_bf16 v[18:33], v[106:109], v[138:141], v[18:33]
	s_waitcnt lgkmcnt(9)
	v_mfma_f32_32x32x16_bf16 v[82:97], v[110:113], v[138:141], v[82:97]
	s_waitcnt lgkmcnt(8)
	v_mfma_f32_32x32x16_bf16 v[34:49], v[118:121], v[138:141], v[34:49]
	s_waitcnt lgkmcnt(7)
	v_mfma_f32_32x32x16_bf16 v[66:81], v[138:141], v[122:125], v[66:81]
	s_waitcnt lgkmcnt(6)
	v_mfma_f32_32x32x16_bf16 v[2:17], v[138:141], v[126:129], v[2:17]
	s_waitcnt lgkmcnt(6)
	s_barrier
	ds_read_b128 v[98:101], v206 offset:52224
	ds_read_b128 v[106:109], v206 offset:56320
	ds_read_b128 v[110:113], v206 offset:60416
	ds_read_b128 v[118:121], v206 offset:64512
	ds_read_b128 v[122:125], v246
	ds_read_b128 v[126:129], v247
	s_waitcnt lgkmcnt(11)
	v_mfma_f32_32x32x16_bf16 v[50:65], v[102:105], v[134:137], v[50:65]
	s_waitcnt lgkmcnt(10)
	v_mfma_f32_32x32x16_bf16 v[18:33], v[114:117], v[134:137], v[18:33]
	s_waitcnt lgkmcnt(9)
	v_mfma_f32_32x32x16_bf16 v[82:97], v[218:221], v[134:137], v[82:97]
	s_waitcnt lgkmcnt(8)
	v_mfma_f32_32x32x16_bf16 v[34:49], v[222:225], v[134:137], v[34:49]
	s_waitcnt lgkmcnt(7)
	v_mfma_f32_32x32x16_bf16 v[66:81], v[134:137], v[226:229], v[66:81]
	s_waitcnt lgkmcnt(6)
	v_mfma_f32_32x32x16_bf16 v[2:17], v[134:137], v[230:233], v[2:17]
	ds_read_b128 v[102:105], v206
	ds_read_b128 v[114:117], v206 offset:4096
	ds_read_b128 v[218:221], v206 offset:8192
	ds_read_b128 v[222:225], v206 offset:12288
	ds_read_b128 v[226:229], v206 offset:16384
	ds_read_b128 v[230:233], v206 offset:20480
	s_waitcnt lgkmcnt(11)
	v_mfma_f32_32x32x16_bf16 v[50:65], v[98:101], v[130:133], v[50:65]
	s_waitcnt lgkmcnt(10)
	v_mfma_f32_32x32x16_bf16 v[18:33], v[106:109], v[130:133], v[18:33]
	s_waitcnt lgkmcnt(9)
	v_mfma_f32_32x32x16_bf16 v[82:97], v[110:113], v[130:133], v[82:97]
	s_waitcnt lgkmcnt(8)
	v_mfma_f32_32x32x16_bf16 v[34:49], v[118:121], v[130:133], v[34:49]
	s_waitcnt lgkmcnt(7)
	v_mfma_f32_32x32x16_bf16 v[66:81], v[130:133], v[122:125], v[66:81]
	s_waitcnt lgkmcnt(6)
	v_mfma_f32_32x32x16_bf16 v[2:17], v[130:133], v[126:129], v[2:17]
	s_waitcnt vmcnt(6)
	ds_write_b128 v208, v[174:177] offset:24576
	s_waitcnt vmcnt(5)
	ds_write_b128 v208, v[182:185] offset:32768
	s_waitcnt vmcnt(4)
	ds_write_b128 v208, v[186:189] offset:40960
	s_lshl_b64 s[42:43], s[2:3], 9
	s_or_b64 s[42:43], s[42:43], s[6:7]
	v_or_b32_e32 v252, s42, v211
	v_lshlrev_b32_e32 v252, 8, v252
	v_lshl_or_b32 v252, v212, 5, v252
	v_or_b32_e32 v252, v252, v1
	v_lshlrev_b32_e32 v252, 2, v252
	global_load_dword v249, v252, s[8:9]
	global_load_dword v248, v252, s[8:9] offset:1024
	global_load_dword v247, v252, s[8:9] offset:2048
	global_load_dword v246, v252, s[8:9] offset:3072
	global_load_dword v245, v252, s[44:45]
	global_load_dword v243, v252, s[44:45] offset:1024
	global_load_dword v241, v252, s[44:45] offset:2048
	global_load_dword v239, v252, s[44:45] offset:3072
	global_load_dword v244, v252, s[46:47]
	global_load_dword v242, v252, s[46:47] offset:1024
	global_load_dword v240, v252, s[46:47] offset:2048
	global_load_dword v238, v252, s[46:47] offset:3072
	global_load_dword v236, v252, s[48:49]
	global_load_dword v234, v252, s[48:49] offset:1024
	global_load_dword v237, v252, s[50:51]
	global_load_dword v235, v252, s[50:51] offset:1024
	ds_read_b128 v[98:101], v206 offset:1024
	ds_read_b128 v[106:109], v206 offset:5120
	ds_read_b128 v[110:113], v206 offset:9216
	ds_read_b128 v[118:121], v206 offset:13312
	ds_read_b128 v[122:125], v206 offset:17408
	ds_read_b128 v[126:129], v206 offset:21504
	s_waitcnt lgkmcnt(14)
	v_mfma_f32_32x32x16_bf16 v[50:65], v[102:105], v[170:173], v[50:65]
	s_waitcnt lgkmcnt(13)
	v_mfma_f32_32x32x16_bf16 v[18:33], v[114:117], v[170:173], v[18:33]
	s_waitcnt lgkmcnt(12)
	v_mfma_f32_32x32x16_bf16 v[82:97], v[218:221], v[170:173], v[82:97]
	s_waitcnt lgkmcnt(11)
	v_mfma_f32_32x32x16_bf16 v[34:49], v[222:225], v[170:173], v[34:49]
	s_waitcnt lgkmcnt(10)
	v_mfma_f32_32x32x16_bf16 v[66:81], v[170:173], v[226:229], v[66:81]
	s_waitcnt lgkmcnt(9)
	v_mfma_f32_32x32x16_bf16 v[2:17], v[170:173], v[230:233], v[2:17]
	ds_read_b128 v[102:105], v206 offset:2048
	ds_read_b128 v[114:117], v206 offset:6144
	ds_read_b128 v[218:221], v206 offset:10240
	ds_read_b128 v[222:225], v206 offset:14336
	ds_read_b128 v[226:229], v206 offset:18432
	ds_read_b128 v[230:233], v206 offset:22528
	s_waitcnt lgkmcnt(11)
	v_mfma_f32_32x32x16_bf16 v[50:65], v[98:101], v[162:165], v[50:65]
	s_waitcnt lgkmcnt(10)
	v_mfma_f32_32x32x16_bf16 v[18:33], v[106:109], v[162:165], v[18:33]
	s_waitcnt lgkmcnt(9)
	v_mfma_f32_32x32x16_bf16 v[82:97], v[110:113], v[162:165], v[82:97]
	s_waitcnt lgkmcnt(8)
	v_mfma_f32_32x32x16_bf16 v[34:49], v[118:121], v[162:165], v[34:49]
	s_waitcnt lgkmcnt(7)
	v_mfma_f32_32x32x16_bf16 v[66:81], v[162:165], v[122:125], v[66:81]
	s_waitcnt lgkmcnt(6)
	v_mfma_f32_32x32x16_bf16 v[2:17], v[162:165], v[126:129], v[2:17]
	s_waitcnt lgkmcnt(6)
	s_barrier
	ds_read_b128 v[98:101], v206 offset:3072
	ds_read_b128 v[106:109], v206 offset:7168
	ds_read_b128 v[110:113], v206 offset:11264
	ds_read_b128 v[118:121], v206 offset:15360
	ds_read_b128 v[122:125], v206 offset:19456
	ds_read_b128 v[126:129], v206 offset:23552
	s_waitcnt lgkmcnt(11)
	v_mfma_f32_32x32x16_bf16 v[50:65], v[102:105], v[154:157], v[50:65]
	s_waitcnt lgkmcnt(10)
	v_mfma_f32_32x32x16_bf16 v[18:33], v[114:117], v[154:157], v[18:33]
	s_waitcnt lgkmcnt(9)
	v_mfma_f32_32x32x16_bf16 v[82:97], v[218:221], v[154:157], v[82:97]
	s_waitcnt lgkmcnt(8)
	v_mfma_f32_32x32x16_bf16 v[34:49], v[222:225], v[154:157], v[34:49]
	s_waitcnt lgkmcnt(7)
	v_mfma_f32_32x32x16_bf16 v[66:81], v[154:157], v[226:229], v[66:81]
	s_waitcnt lgkmcnt(6)
	v_mfma_f32_32x32x16_bf16 v[2:17], v[154:157], v[230:233], v[2:17]
	ds_read_b128 v[102:105], v206 offset:24576
	ds_read_b128 v[114:117], v206 offset:28672
	ds_read_b128 v[218:221], v206 offset:32768
	ds_read_b128 v[222:225], v206 offset:36864
	ds_read_b128 v[226:229], v206 offset:40960
	ds_read_b128 v[230:233], v206 offset:45056
	s_waitcnt lgkmcnt(11)
	v_mfma_f32_32x32x16_bf16 v[50:65], v[98:101], v[146:149], v[50:65]
	s_waitcnt lgkmcnt(10)
	v_mfma_f32_32x32x16_bf16 v[18:33], v[106:109], v[146:149], v[18:33]
	s_waitcnt lgkmcnt(9)
	v_mfma_f32_32x32x16_bf16 v[82:97], v[110:113], v[146:149], v[82:97]
	s_waitcnt lgkmcnt(8)
	v_mfma_f32_32x32x16_bf16 v[34:49], v[118:121], v[146:149], v[34:49]
	s_waitcnt lgkmcnt(7)
	v_mfma_f32_32x32x16_bf16 v[66:81], v[146:149], v[122:125], v[66:81]
	s_waitcnt lgkmcnt(6)
	v_mfma_f32_32x32x16_bf16 v[2:17], v[146:149], v[126:129], v[2:17]
	ds_read_b128 v[98:101], v206 offset:25600
	ds_read_b128 v[106:109], v206 offset:29696
	ds_read_b128 v[110:113], v206 offset:33792
	ds_read_b128 v[118:121], v206 offset:37888
	ds_read_b128 v[122:125], v206 offset:41984
	ds_read_b128 v[126:129], v206 offset:46080
	s_waitcnt vmcnt(19) lgkmcnt(11)
	v_mfma_f32_32x32x16_bf16 v[50:65], v[102:105], v[178:181], v[50:65]
	s_waitcnt lgkmcnt(10)
	v_mfma_f32_32x32x16_bf16 v[18:33], v[114:117], v[178:181], v[18:33]
	s_waitcnt lgkmcnt(9)
	v_mfma_f32_32x32x16_bf16 v[82:97], v[218:221], v[178:181], v[82:97]
	s_waitcnt lgkmcnt(8)
	v_mfma_f32_32x32x16_bf16 v[34:49], v[222:225], v[178:181], v[34:49]
	s_waitcnt lgkmcnt(7)
	v_mfma_f32_32x32x16_bf16 v[66:81], v[178:181], v[226:229], v[66:81]
	s_waitcnt lgkmcnt(6)
	v_mfma_f32_32x32x16_bf16 v[2:17], v[178:181], v[230:233], v[2:17]
	ds_read_b128 v[102:105], v206 offset:26624
	ds_read_b128 v[114:117], v206 offset:30720
	ds_read_b128 v[218:221], v206 offset:34816
	ds_read_b128 v[222:225], v206 offset:38912
	ds_read_b128 v[226:229], v206 offset:43008
	ds_read_b128 v[230:233], v206 offset:47104
	s_waitcnt vmcnt(18) lgkmcnt(11)
	v_mfma_f32_32x32x16_bf16 v[50:65], v[98:101], v[166:169], v[50:65]
	s_waitcnt lgkmcnt(10)
	v_mfma_f32_32x32x16_bf16 v[18:33], v[106:109], v[166:169], v[18:33]
	s_waitcnt lgkmcnt(9)
	v_mfma_f32_32x32x16_bf16 v[82:97], v[110:113], v[166:169], v[82:97]
	s_waitcnt lgkmcnt(8)
	v_mfma_f32_32x32x16_bf16 v[34:49], v[118:121], v[166:169], v[34:49]
	s_waitcnt lgkmcnt(7)
	v_mfma_f32_32x32x16_bf16 v[66:81], v[166:169], v[122:125], v[66:81]
	s_waitcnt lgkmcnt(6)
	v_mfma_f32_32x32x16_bf16 v[2:17], v[166:169], v[126:129], v[2:17]
	s_waitcnt lgkmcnt(6)
	s_barrier
	ds_read_b128 v[98:101], v206 offset:27648
	ds_read_b128 v[106:109], v206 offset:31744
	ds_read_b128 v[110:113], v206 offset:35840
	ds_read_b128 v[118:121], v206 offset:39936
	ds_read_b128 v[122:125], v206 offset:44032
	ds_read_b128 v[126:129], v206 offset:48128
	s_waitcnt vmcnt(17) lgkmcnt(11)
	v_mfma_f32_32x32x16_bf16 v[50:65], v[102:105], v[158:161], v[50:65]
	s_waitcnt lgkmcnt(10)
	v_mfma_f32_32x32x16_bf16 v[18:33], v[114:117], v[158:161], v[18:33]
	s_waitcnt lgkmcnt(9)
	v_mfma_f32_32x32x16_bf16 v[82:97], v[218:221], v[158:161], v[82:97]
	s_waitcnt lgkmcnt(8)
	v_mfma_f32_32x32x16_bf16 v[34:49], v[222:225], v[158:161], v[34:49]
	s_waitcnt lgkmcnt(7)
	v_mfma_f32_32x32x16_bf16 v[66:81], v[158:161], v[226:229], v[66:81]
	s_waitcnt lgkmcnt(6)
	v_mfma_f32_32x32x16_bf16 v[2:17], v[158:161], v[230:233], v[2:17]
	global_load_dword v232, v252, s[48:49] offset:2048
	global_load_dword v230, v252, s[48:49] offset:3072
	global_load_dword v233, v252, s[50:51] offset:2048
	global_load_dword v231, v252, s[50:51] offset:3072
	global_load_dword v228, v252, s[52:53]
	global_load_dword v226, v252, s[52:53] offset:1024
	global_load_dword v224, v252, s[52:53] offset:2048
	global_load_dword v222, v252, s[52:53] offset:3072
	global_load_dword v229, v252, s[54:55]
	global_load_dword v227, v252, s[54:55] offset:1024
	global_load_dword v225, v252, s[54:55] offset:2048
	global_load_dword v223, v252, s[54:55] offset:3072
	global_load_dword v221, v252, s[56:57]
	global_load_dword v220, v252, s[56:57] offset:1024
	global_load_dword v219, v252, s[56:57] offset:2048
	global_load_dword v218, v252, s[56:57] offset:3072
	s_waitcnt vmcnt(32) lgkmcnt(5)
	v_mfma_f32_32x32x16_bf16 v[50:65], v[98:101], v[150:153], v[50:65]
	s_waitcnt lgkmcnt(4)
	v_mfma_f32_32x32x16_bf16 v[18:33], v[106:109], v[150:153], v[18:33]
	s_waitcnt lgkmcnt(3)
	v_mfma_f32_32x32x16_bf16 v[82:97], v[110:113], v[150:153], v[82:97]
	s_waitcnt lgkmcnt(2)
	v_mfma_f32_32x32x16_bf16 v[34:49], v[118:121], v[150:153], v[34:49]
	s_waitcnt lgkmcnt(1)
	v_mfma_f32_32x32x16_bf16 v[66:81], v[150:153], v[122:125], v[66:81]
	s_waitcnt lgkmcnt(0)
	v_mfma_f32_32x32x16_bf16 v[2:17], v[150:153], v[126:129], v[2:17]
	s_barrier
	s_and_b64 vcc, exec, s[18:19]
	s_cbranch_vccnz .LBB3_141
	v_or_b32_e32 v100, v215, v214
	v_ashrrev_i32_e32 v101, 31, v100
	v_or_b32_e32 v102, v216, v214
	v_lshlrev_b64 v[100:101], 10, v[100:101]
	v_ashrrev_i32_e32 v103, 31, v102
	v_lshl_add_u64 v[100:101], v[202:203], 0, v[100:101]
	v_lshlrev_b64 v[102:103], 10, v[102:103]
	v_lshl_add_u64 v[102:103], v[202:203], 0, v[102:103]
	global_load_dwordx4 v[190:193], v[100:101], off
	global_load_dwordx4 v[194:197], v[102:103], off
	v_or_b32_e32 v100, v217, v214
	v_or_b32_e32 v104, 4, v214
	v_ashrrev_i32_e32 v101, 31, v100
	v_or_b32_e32 v102, v104, v215
	v_lshlrev_b64 v[100:101], 10, v[100:101]
	v_ashrrev_i32_e32 v103, 31, v102
	v_add_u32_e32 v98, s28, v212
	v_lshl_add_u64 v[100:101], v[202:203], 0, v[100:101]
	v_lshlrev_b64 v[102:103], 10, v[102:103]
	v_ashrrev_i32_e32 v99, 31, v98
	v_lshl_add_u64 v[102:103], v[202:203], 0, v[102:103]
	global_load_dwordx4 v[198:201], v[100:101], off
	global_load_dwordx4 v[174:177], v[102:103], off
	v_or_b32_e32 v100, v216, v104
	v_lshlrev_b64 v[98:99], 15, v[98:99]
	v_ashrrev_i32_e32 v101, 31, v100
	v_or_b32_e32 v102, v217, v104
	v_lshl_add_u64 v[98:99], s[10:11], 0, v[98:99]
	v_lshlrev_b64 v[100:101], 10, v[100:101]
	v_ashrrev_i32_e32 v103, 31, v102
	v_lshl_add_u64 v[98:99], v[98:99], 0, v[206:207]
	v_lshl_add_u64 v[100:101], v[202:203], 0, v[100:101]
	v_lshlrev_b64 v[102:103], 10, v[102:103]
	v_lshl_add_u64 v[102:103], v[202:203], 0, v[102:103]
	global_load_dwordx4 v[182:185], v[100:101], off
	global_load_dwordx4 v[186:189], v[102:103], off
	global_load_dwordx4 v[170:173], v[98:99], off
	global_load_dwordx4 v[162:165], v[98:99], off offset:1024
	global_load_dwordx4 v[154:157], v[98:99], off offset:2048
	global_load_dwordx4 v[146:149], v[98:99], off offset:3072
	v_add_co_u32_e32 v100, vcc, 0x1000, v98
	s_nop 1
	v_addc_co_u32_e32 v101, vcc, 0, v99, vcc
	v_add_co_u32_e32 v98, vcc, 0x2000, v98
	global_load_dwordx4 v[178:181], v[100:101], off
	global_load_dwordx4 v[166:169], v[100:101], off offset:1024
	global_load_dwordx4 v[158:161], v[100:101], off offset:2048
	global_load_dwordx4 v[150:153], v[100:101], off offset:3072
	v_addc_co_u32_e32 v99, vcc, 0, v99, vcc
	global_load_dwordx4 v[142:145], v[98:99], off
	global_load_dwordx4 v[138:141], v[98:99], off offset:1024
	global_load_dwordx4 v[134:137], v[98:99], off offset:2048
	global_load_dwordx4 v[130:133], v[98:99], off offset:3072
	s_branch .LBB3_141
